# speedup vs baseline: 1.0879x; 1.0247x over previous
.LBB0_75:
	s_and_b64 vcc, exec, s[4:5]
	s_cbranch_vccz .LBB0_86
	s_lshl_b32 s6, s2, 10
	s_cmpk_gt_i32 s6, 0xfff
	s_cbranch_scc1 .LBB0_86
	v_or_b32_e32 v2, s6, v0
	v_ashrrev_i32_e32 v4, 9, v2
	s_waitcnt lgkmcnt(0)
	v_lshrrev_b32_e32 v3, 30, v4
	s_sub_i32 s4, s3, 21
	s_mov_b32 s5, 0
	v_add_u32_e32 v3, v4, v3
	s_lshl_b64 s[0:1], s[4:5], 2
	v_bfe_u32 v7, v0, 3, 5
	v_ashrrev_i32_e32 v5, 2, v3
	s_add_u32 s0, s18, s0
	v_lshlrev_b32_e32 v1, 1, v0
	v_lshl_or_b32 v3, v5, 5, v7
	s_addc_u32 s1, s19, s1
	v_and_b32_e32 v1, 8, v1
	v_and_b32_e32 v6, 3, v0
	v_cmp_gt_i32_e32 vcc, 64, v3
	v_mov_b32_e32 v8, 0
	v_mov_b32_e32 v9, 0
	v_mov_b32_e32 v100, 0
	s_and_saveexec_b64 s[6:7], vcc
	s_cbranch_execz .LBB0_79
	v_mul_i32_i24_e32 v5, 4, v5
	v_sub_u32_e32 v4, v4, v5
	v_lshrrev_b32_e32 v5, 6, v0
	v_and_b32_e32 v5, 4, v5
	v_lshl_or_b32 v4, v4, 4, v5
	v_or3_b32 v4, v4, v1, v6
	v_lshl_add_u32 v4, v4, 3, v4
	v_ashrrev_i32_e32 v5, 31, v4
	v_lshl_add_u64 v[4:5], v[4:5], 2, s[0:1]
	s_movk_i32 s5, 0x900
	v_mad_i64_i32 v[4:5], s[8:9], v3, s5, v[4:5]
	global_load_dword v100, v[4:5], off
.LBB0_79:
	s_or_b64 exec, exec, s[6:7]
	s_lshl_b32 s4, s4, 13
	s_add_u32 s4, s22, s4
	s_addc_u32 s5, s23, 0
	v_ashrrev_i32_e32 v3, 31, v2
	v_lshl_add_u64 v[10:11], v[2:3], 1, s[4:5]
	s_mov_b64 s[4:5], 0x41000
	v_lshl_add_u64 v[4:5], v[10:11], 0, s[4:5]
	v_add_co_u32_e32 v10, vcc, 0x41000, v10
	s_nop 1
	v_addc_co_u32_e32 v11, vcc, 0, v11, vcc
	v_mov_b32_e32 v104, v10
	v_mov_b32_e32 v105, v11
	v_add_u32_e32 v9, 0x100, v2
	v_ashrrev_i32_e32 v10, 9, v9
	v_lshrrev_b32_e32 v3, 30, v10
	v_add_u32_e32 v3, v10, v3
	v_ashrrev_i32_e32 v11, 2, v3
	v_lshl_or_b32 v3, v11, 5, v7
	v_cmp_gt_i32_e32 vcc, 64, v3
	v_mov_b32_e32 v101, 0
	s_and_saveexec_b64 s[4:5], vcc
	s_cbranch_execz .LBB0_81
	v_mul_i32_i24_e32 v8, 4, v11
	v_lshrrev_b32_e32 v9, 6, v9
	v_sub_u32_e32 v8, v10, v8
	v_and_b32_e32 v9, 4, v9
	v_lshl_or_b32 v8, v8, 4, v9
	v_or3_b32 v8, v8, v1, v6
	v_lshl_add_u32 v8, v8, 3, v8
	v_ashrrev_i32_e32 v9, 31, v8
	v_lshl_add_u64 v[8:9], v[8:9], 2, s[0:1]
	s_movk_i32 s6, 0x900
	v_mad_i64_i32 v[8:9], s[6:7], v3, s6, v[8:9]
	global_load_dword v101, v[8:9], off
.LBB0_81:
	s_or_b64 exec, exec, s[4:5]
	v_add_u32_e32 v3, 0x200, v2
	v_ashrrev_i32_e32 v9, 9, v3
	v_lshrrev_b32_e32 v3, 30, v9
	v_add_u32_e32 v3, v9, v3
	v_ashrrev_i32_e32 v10, 2, v3
	v_mov_b32_e32 v106, v4
	v_mov_b32_e32 v107, v5
	v_lshl_or_b32 v8, v10, 5, v7
	v_cmp_gt_i32_e32 vcc, 64, v8
	v_mov_b32_e32 v3, 0
	v_mov_b32_e32 v11, 0
	v_mov_b32_e32 v102, 0
	s_and_saveexec_b64 s[4:5], vcc
	s_cbranch_execz .LBB0_83
	v_mul_i32_i24_e32 v10, 4, v10
	v_sub_u32_e32 v9, v9, v10
	v_lshrrev_b32_e32 v10, 6, v0
	v_and_b32_e32 v10, 4, v10
	v_lshl_or_b32 v9, v9, 4, v10
	v_or3_b32 v9, v9, v1, v6
	v_lshl_add_u32 v10, v9, 3, v9
	v_ashrrev_i32_e32 v11, 31, v10
	v_lshl_add_u64 v[10:11], v[10:11], 2, s[0:1]
	s_movk_i32 s6, 0x900
	v_mad_i64_i32 v[8:9], s[6:7], v8, s6, v[10:11]
	global_load_dword v102, v[8:9], off
.LBB0_83:
	s_or_b64 exec, exec, s[4:5]
	v_add_u32_e32 v8, 0x300, v2
	v_ashrrev_i32_e32 v9, 9, v8
	v_lshrrev_b32_e32 v2, 30, v9
	v_add_u32_e32 v2, v9, v2
	v_ashrrev_i32_e32 v10, 2, v2
	v_lshl_or_b32 v2, v10, 5, v7
	v_cmp_gt_i32_e32 vcc, 64, v2
	v_mov_b32_e32 v108, v4
	v_mov_b32_e32 v109, v5
	v_mov_b32_e32 v103, 0
	s_and_saveexec_b64 s[4:5], vcc
	s_cbranch_execz .LBB0_85
	v_mul_i32_i24_e32 v3, 4, v10
	v_lshrrev_b32_e32 v7, 6, v8
	v_sub_u32_e32 v3, v9, v3
	v_and_b32_e32 v7, 4, v7
	v_lshl_or_b32 v3, v3, 4, v7
	v_or3_b32 v1, v3, v1, v6
	v_lshl_add_u32 v6, v1, 3, v1
	v_ashrrev_i32_e32 v7, 31, v6
	v_lshl_add_u64 v[6:7], v[6:7], 2, s[0:1]
	s_movk_i32 s0, 0x900
	v_mad_i64_i32 v[2:3], s[0:1], v2, s0, v[6:7]
	global_load_dword v103, v[2:3], off
.LBB0_85:
	s_or_b64 exec, exec, s[4:5]
	s_waitcnt vmcnt(0)
	v_cvt_f16_f32_e32 v100, v100
	v_cvt_f16_f32_e32 v101, v101
	v_cvt_f16_f32_e32 v102, v102
	v_cvt_f16_f32_e32 v103, v103
	global_store_short v[104:105], v100, off
	global_store_short v[106:107], v101, off offset:512
	global_store_short v[108:109], v102, off offset:1024
	global_store_short v[4:5], v103, off offset:1536

.LBB0_87:
	s_andn2_b64 vcc, exec, s[4:5]
	s_cbranch_vccnz .LBB0_98
	s_lshl_b32 s0, s2, 10
	s_cmpk_gt_i32 s0, 0xfff
	s_cbranch_scc1 .LBB0_98
	v_or_b32_e32 v2, s0, v0
	s_waitcnt lgkmcnt(0)
	v_ashrrev_i32_e32 v3, 9, v2
	v_lshrrev_b32_e32 v4, 30, v3
	v_add_u32_e32 v4, v3, v4
	v_bfe_u32 v9, v0, 3, 5
	v_ashrrev_i32_e32 v6, 2, v4
	v_lshlrev_b32_e32 v1, 1, v0
	v_lshl_or_b32 v4, v6, 5, v9
	v_and_b32_e32 v1, 8, v1
	v_and_b32_e32 v8, 3, v0
	v_cmp_gt_i32_e32 vcc, 64, v4
	v_mov_b32_e32 v7, 0
	v_mov_b32_e32 v5, 0
	v_mov_b32_e32 v100, 0
	s_and_saveexec_b64 s[0:1], vcc
	s_cbranch_execz .LBB0_91
	v_mul_i32_i24_e32 v5, 4, v6
	v_sub_u32_e32 v3, v3, v5
	v_lshrrev_b32_e32 v5, 6, v0
	v_and_b32_e32 v5, 4, v5
	v_lshl_or_b32 v3, v3, 4, v5
	v_or3_b32 v10, v3, v1, v8
	v_ashrrev_i32_e32 v11, 31, v10
	v_ashrrev_i32_e32 v5, 31, v4
	v_lshl_add_u64 v[10:11], v[10:11], 2, s[16:17]
	v_lshlrev_b64 v[4:5], 8, v[4:5]
	v_lshl_add_u64 v[4:5], v[10:11], 0, v[4:5]
	global_load_dword v100, v[4:5], off
.LBB0_91:
	s_or_b64 exec, exec, s[0:1]
	s_add_u32 s0, s22, 0x3f000
	s_addc_u32 s1, s23, 0
	v_ashrrev_i32_e32 v3, 31, v2
	v_add_u32_e32 v4, 0x100, v2
	v_lshl_add_u64 v[10:11], v[2:3], 1, s[0:1]
	v_ashrrev_i32_e32 v3, 9, v4
	v_mov_b32_e32 v104, v10
	v_mov_b32_e32 v105, v11
	v_lshrrev_b32_e32 v5, 30, v3
	v_add_u32_e32 v5, v3, v5
	v_ashrrev_i32_e32 v5, 2, v5
	v_lshl_or_b32 v6, v5, 5, v9
	v_cmp_gt_i32_e32 vcc, 64, v6
	v_mov_b32_e32 v101, 0
	s_and_saveexec_b64 s[4:5], vcc
	s_cbranch_execz .LBB0_93
	v_mul_i32_i24_e32 v5, 4, v5
	v_sub_u32_e32 v3, v3, v5
	v_lshrrev_b32_e32 v5, 6, v4
	v_and_b32_e32 v5, 4, v5
	v_lshl_or_b32 v3, v3, 4, v5
	v_or3_b32 v10, v3, v1, v8
	v_ashrrev_i32_e32 v11, 31, v10
	v_ashrrev_i32_e32 v7, 31, v6
	v_lshl_add_u64 v[10:11], v[10:11], 2, s[16:17]
	v_lshlrev_b64 v[6:7], 8, v[6:7]
	v_lshl_add_u64 v[6:7], v[10:11], 0, v[6:7]
	global_load_dword v101, v[6:7], off
.LBB0_93:
	s_or_b64 exec, exec, s[4:5]
	v_ashrrev_i32_e32 v5, 31, v4
	v_lshl_add_u64 v[4:5], v[4:5], 1, s[0:1]
	v_mov_b32_e32 v106, v4
	v_mov_b32_e32 v107, v5
	v_add_u32_e32 v4, 0x200, v2
	v_ashrrev_i32_e32 v3, 9, v4
	v_lshrrev_b32_e32 v5, 30, v3
	v_add_u32_e32 v5, v3, v5
	v_ashrrev_i32_e32 v5, 2, v5
	v_lshl_or_b32 v6, v5, 5, v9
	v_cmp_gt_i32_e32 vcc, 64, v6
	v_mov_b32_e32 v10, 0
	v_mov_b32_e32 v7, 0
	v_mov_b32_e32 v102, 0
	s_and_saveexec_b64 s[4:5], vcc
	s_cbranch_execz .LBB0_95
	v_mul_i32_i24_e32 v5, 4, v5
	v_sub_u32_e32 v3, v3, v5
	v_lshrrev_b32_e32 v5, 6, v0
	v_and_b32_e32 v5, 4, v5
	v_lshl_or_b32 v3, v3, 4, v5
	v_or3_b32 v12, v3, v1, v8
	v_ashrrev_i32_e32 v13, 31, v12
	v_ashrrev_i32_e32 v7, 31, v6
	v_lshl_add_u64 v[12:13], v[12:13], 2, s[16:17]
	v_lshlrev_b64 v[6:7], 8, v[6:7]
	v_lshl_add_u64 v[6:7], v[12:13], 0, v[6:7]
	global_load_dword v102, v[6:7], off
.LBB0_95:
	s_or_b64 exec, exec, s[4:5]
	v_ashrrev_i32_e32 v5, 31, v4
	v_add_u32_e32 v2, 0x300, v2
	v_lshl_add_u64 v[4:5], v[4:5], 1, s[0:1]
	v_ashrrev_i32_e32 v3, 9, v2
	v_mov_b32_e32 v108, v4
	v_mov_b32_e32 v109, v5
	v_lshrrev_b32_e32 v4, 30, v3
	v_add_u32_e32 v4, v3, v4
	v_ashrrev_i32_e32 v5, 2, v4
	v_lshl_or_b32 v4, v5, 5, v9
	v_cmp_gt_i32_e32 vcc, 64, v4
	v_mov_b32_e32 v103, 0
	s_and_saveexec_b64 s[4:5], vcc
	s_cbranch_execz .LBB0_97
	v_mul_i32_i24_e32 v5, 4, v5
	v_sub_u32_e32 v3, v3, v5
	v_lshrrev_b32_e32 v5, 6, v2
	v_and_b32_e32 v5, 4, v5
	v_lshl_or_b32 v3, v3, 4, v5
	v_or3_b32 v6, v3, v1, v8
	v_ashrrev_i32_e32 v7, 31, v6
	v_ashrrev_i32_e32 v5, 31, v4
	v_lshl_add_u64 v[6:7], v[6:7], 2, s[16:17]
	v_lshlrev_b64 v[4:5], 8, v[4:5]
	v_lshl_add_u64 v[4:5], v[6:7], 0, v[4:5]
	global_load_dword v103, v[4:5], off
.LBB0_97:
	s_or_b64 exec, exec, s[4:5]
	v_ashrrev_i32_e32 v3, 31, v2
	v_lshl_add_u64 v[2:3], v[2:3], 1, s[0:1]
	s_waitcnt vmcnt(0)
	v_cvt_f16_f32_e32 v100, v100
	v_cvt_f16_f32_e32 v101, v101
	v_cvt_f16_f32_e32 v102, v102
	v_cvt_f16_f32_e32 v103, v103
	global_store_short v[104:105], v100, off
	global_store_short v[106:107], v101, off
	global_store_short v[108:109], v102, off
	global_store_short v[2:3], v103, off

.LBB0_99:
	s_andn2_b64 vcc, exec, s[4:5]
	s_cbranch_vccnz .LBB0_110
	s_lshl_b32 s0, s2, 10
	s_cmpk_gt_i32 s0, 0xfff
	s_cbranch_scc1 .LBB0_110
	v_or_b32_e32 v2, s0, v0
	s_waitcnt lgkmcnt(0)
	v_ashrrev_i32_e32 v3, 9, v2
	v_lshrrev_b32_e32 v4, 30, v3
	v_add_u32_e32 v4, v3, v4
	v_bfe_u32 v9, v0, 3, 5
	v_ashrrev_i32_e32 v6, 2, v4
	v_lshlrev_b32_e32 v1, 1, v0
	v_lshl_or_b32 v4, v6, 5, v9
	v_and_b32_e32 v1, 8, v1
	v_and_b32_e32 v8, 3, v0
	v_cmp_gt_i32_e32 vcc, 64, v4
	v_mov_b32_e32 v7, 0
	v_mov_b32_e32 v5, 0
	v_mov_b32_e32 v100, 0
	s_and_saveexec_b64 s[0:1], vcc
	s_cbranch_execz .LBB0_103
	v_mul_i32_i24_e32 v5, 4, v6
	v_sub_u32_e32 v3, v3, v5
	v_lshrrev_b32_e32 v5, 6, v0
	v_and_b32_e32 v5, 4, v5
	v_lshl_or_b32 v3, v3, 4, v5
	v_or3_b32 v10, v3, v1, v8
	v_ashrrev_i32_e32 v11, 31, v10
	v_ashrrev_i32_e32 v5, 31, v4
	v_lshl_add_u64 v[10:11], v[10:11], 2, s[14:15]
	v_lshlrev_b64 v[4:5], 8, v[4:5]
	v_lshl_add_u64 v[4:5], v[10:11], 0, v[4:5]
	global_load_dword v100, v[4:5], off
.LBB0_103:
	s_or_b64 exec, exec, s[0:1]
	s_add_u32 s0, s22, 0x3d000
	s_addc_u32 s1, s23, 0
	v_ashrrev_i32_e32 v3, 31, v2
	v_add_u32_e32 v4, 0x100, v2
	v_lshl_add_u64 v[10:11], v[2:3], 1, s[0:1]
	v_ashrrev_i32_e32 v3, 9, v4
	v_mov_b32_e32 v104, v10
	v_mov_b32_e32 v105, v11
	v_lshrrev_b32_e32 v5, 30, v3
	v_add_u32_e32 v5, v3, v5
	v_ashrrev_i32_e32 v5, 2, v5
	v_lshl_or_b32 v6, v5, 5, v9
	v_cmp_gt_i32_e32 vcc, 64, v6
	v_mov_b32_e32 v101, 0
	s_and_saveexec_b64 s[4:5], vcc
	s_cbranch_execz .LBB0_105
	v_mul_i32_i24_e32 v5, 4, v5
	v_sub_u32_e32 v3, v3, v5
	v_lshrrev_b32_e32 v5, 6, v4
	v_and_b32_e32 v5, 4, v5
	v_lshl_or_b32 v3, v3, 4, v5
	v_or3_b32 v10, v3, v1, v8
	v_ashrrev_i32_e32 v11, 31, v10
	v_ashrrev_i32_e32 v7, 31, v6
	v_lshl_add_u64 v[10:11], v[10:11], 2, s[14:15]
	v_lshlrev_b64 v[6:7], 8, v[6:7]
	v_lshl_add_u64 v[6:7], v[10:11], 0, v[6:7]
	global_load_dword v101, v[6:7], off
.LBB0_105:
	s_or_b64 exec, exec, s[4:5]
	v_ashrrev_i32_e32 v5, 31, v4
	v_lshl_add_u64 v[4:5], v[4:5], 1, s[0:1]
	v_mov_b32_e32 v106, v4
	v_mov_b32_e32 v107, v5
	v_add_u32_e32 v4, 0x200, v2
	v_ashrrev_i32_e32 v3, 9, v4
	v_lshrrev_b32_e32 v5, 30, v3
	v_add_u32_e32 v5, v3, v5
	v_ashrrev_i32_e32 v5, 2, v5
	v_lshl_or_b32 v6, v5, 5, v9
	v_cmp_gt_i32_e32 vcc, 64, v6
	v_mov_b32_e32 v10, 0
	v_mov_b32_e32 v7, 0
	v_mov_b32_e32 v102, 0
	s_and_saveexec_b64 s[4:5], vcc
	s_cbranch_execz .LBB0_107
	v_mul_i32_i24_e32 v5, 4, v5
	v_sub_u32_e32 v3, v3, v5
	v_lshrrev_b32_e32 v5, 6, v0
	v_and_b32_e32 v5, 4, v5
	v_lshl_or_b32 v3, v3, 4, v5
	v_or3_b32 v12, v3, v1, v8
	v_ashrrev_i32_e32 v13, 31, v12
	v_ashrrev_i32_e32 v7, 31, v6
	v_lshl_add_u64 v[12:13], v[12:13], 2, s[14:15]
	v_lshlrev_b64 v[6:7], 8, v[6:7]
	v_lshl_add_u64 v[6:7], v[12:13], 0, v[6:7]
	global_load_dword v102, v[6:7], off
.LBB0_107:
	s_or_b64 exec, exec, s[4:5]
	v_ashrrev_i32_e32 v5, 31, v4
	v_add_u32_e32 v2, 0x300, v2
	v_lshl_add_u64 v[4:5], v[4:5], 1, s[0:1]
	v_ashrrev_i32_e32 v3, 9, v2
	v_mov_b32_e32 v108, v4
	v_mov_b32_e32 v109, v5
	v_lshrrev_b32_e32 v4, 30, v3
	v_add_u32_e32 v4, v3, v4
	v_ashrrev_i32_e32 v5, 2, v4
	v_lshl_or_b32 v4, v5, 5, v9
	v_cmp_gt_i32_e32 vcc, 64, v4
	v_mov_b32_e32 v103, 0
	s_and_saveexec_b64 s[4:5], vcc
	s_cbranch_execz .LBB0_109
	v_mul_i32_i24_e32 v5, 4, v5
	v_sub_u32_e32 v3, v3, v5
	v_lshrrev_b32_e32 v5, 6, v2
	v_and_b32_e32 v5, 4, v5
	v_lshl_or_b32 v3, v3, 4, v5
	v_or3_b32 v6, v3, v1, v8
	v_ashrrev_i32_e32 v7, 31, v6
	v_ashrrev_i32_e32 v5, 31, v4
	v_lshl_add_u64 v[6:7], v[6:7], 2, s[14:15]
	v_lshlrev_b64 v[4:5], 8, v[4:5]
	v_lshl_add_u64 v[4:5], v[6:7], 0, v[4:5]
	global_load_dword v103, v[4:5], off

.LBB0_111:
	s_andn2_b64 vcc, exec, s[4:5]
	s_cbranch_vccnz .LBB0_135
	s_cmp_gt_i32 s3, 17
	s_mov_b64 s[0:1], -1
	s_cbranch_scc0 .LBB0_124
	s_lshl_b32 s0, s2, 10
	s_cmpk_gt_i32 s0, 0x7ff
	s_cbranch_scc1 .LBB0_123
	v_or_b32_e32 v2, s0, v0
	s_waitcnt lgkmcnt(0)
	v_ashrrev_i32_e32 v3, 9, v2
	v_lshrrev_b32_e32 v4, 30, v3
	v_add_u32_e32 v4, v3, v4
	v_bfe_u32 v9, v0, 3, 5
	v_ashrrev_i32_e32 v6, 2, v4
	v_lshlrev_b32_e32 v1, 1, v0
	v_lshl_or_b32 v4, v6, 5, v9
	v_and_b32_e32 v1, 8, v1
	v_and_b32_e32 v8, 3, v0
	v_cmp_gt_i32_e32 vcc, 16, v4
	v_mov_b32_e32 v7, 0
	v_mov_b32_e32 v5, 0
	v_mov_b32_e32 v100, 0
	s_and_saveexec_b64 s[0:1], vcc
	s_cbranch_execz .LBB0_116
	v_mul_i32_i24_e32 v5, 4, v6
	v_sub_u32_e32 v3, v3, v5
	v_lshrrev_b32_e32 v5, 6, v0
	v_and_b32_e32 v5, 4, v5
	v_lshl_or_b32 v3, v3, 4, v5
	v_or3_b32 v10, v3, v1, v8
	v_ashrrev_i32_e32 v11, 31, v10
	v_lshlrev_b64 v[10:11], 6, v[10:11]
	v_ashrrev_i32_e32 v5, 31, v4
	v_lshl_add_u64 v[10:11], s[12:13], 0, v[10:11]
	v_lshl_add_u64 v[4:5], v[4:5], 2, v[10:11]
	global_load_dword v100, v[4:5], off
.LBB0_116:
	s_or_b64 exec, exec, s[0:1]
	s_add_u32 s0, s22, 0x3c000
	s_addc_u32 s1, s23, 0
	v_ashrrev_i32_e32 v3, 31, v2
	v_add_u32_e32 v4, 0x100, v2
	v_lshl_add_u64 v[10:11], v[2:3], 1, s[0:1]
	v_ashrrev_i32_e32 v3, 9, v4
	v_mov_b32_e32 v104, v10
	v_mov_b32_e32 v105, v11
	v_lshrrev_b32_e32 v5, 30, v3
	v_add_u32_e32 v5, v3, v5
	v_ashrrev_i32_e32 v5, 2, v5
	v_lshl_or_b32 v6, v5, 5, v9
	v_cmp_gt_i32_e32 vcc, 16, v6
	v_mov_b32_e32 v101, 0
	s_and_saveexec_b64 s[4:5], vcc
	s_cbranch_execz .LBB0_118
	v_mul_i32_i24_e32 v5, 4, v5
	v_sub_u32_e32 v3, v3, v5
	v_lshrrev_b32_e32 v5, 6, v4
	v_and_b32_e32 v5, 4, v5
	v_lshl_or_b32 v3, v3, 4, v5
	v_or3_b32 v10, v3, v1, v8
	v_ashrrev_i32_e32 v11, 31, v10
	v_lshlrev_b64 v[10:11], 6, v[10:11]
	v_ashrrev_i32_e32 v7, 31, v6
	v_lshl_add_u64 v[10:11], s[12:13], 0, v[10:11]
	v_lshl_add_u64 v[6:7], v[6:7], 2, v[10:11]
	global_load_dword v101, v[6:7], off
.LBB0_118:
	s_or_b64 exec, exec, s[4:5]
	v_ashrrev_i32_e32 v5, 31, v4
	v_lshl_add_u64 v[4:5], v[4:5], 1, s[0:1]
	v_mov_b32_e32 v106, v4
	v_mov_b32_e32 v107, v5
	v_add_u32_e32 v4, 0x200, v2
	v_ashrrev_i32_e32 v3, 9, v4
	v_lshrrev_b32_e32 v5, 30, v3
	v_add_u32_e32 v5, v3, v5
	v_ashrrev_i32_e32 v5, 2, v5
	v_lshl_or_b32 v6, v5, 5, v9
	v_cmp_gt_i32_e32 vcc, 16, v6
	v_mov_b32_e32 v10, 0
	v_mov_b32_e32 v7, 0
	v_mov_b32_e32 v102, 0
	s_and_saveexec_b64 s[4:5], vcc
	s_cbranch_execz .LBB0_120
	v_mul_i32_i24_e32 v5, 4, v5
	v_sub_u32_e32 v3, v3, v5
	v_lshrrev_b32_e32 v5, 6, v0
	v_and_b32_e32 v5, 4, v5
	v_lshl_or_b32 v3, v3, 4, v5
	v_or3_b32 v12, v3, v1, v8
	v_ashrrev_i32_e32 v13, 31, v12
	v_lshlrev_b64 v[12:13], 6, v[12:13]
	v_ashrrev_i32_e32 v7, 31, v6
	v_lshl_add_u64 v[12:13], s[12:13], 0, v[12:13]
	v_lshl_add_u64 v[6:7], v[6:7], 2, v[12:13]
	global_load_dword v102, v[6:7], off
.LBB0_120:
	s_or_b64 exec, exec, s[4:5]
	v_ashrrev_i32_e32 v5, 31, v4
	v_add_u32_e32 v2, 0x300, v2
	v_lshl_add_u64 v[4:5], v[4:5], 1, s[0:1]
	v_ashrrev_i32_e32 v3, 9, v2
	v_mov_b32_e32 v108, v4
	v_mov_b32_e32 v109, v5
	v_lshrrev_b32_e32 v4, 30, v3
	v_add_u32_e32 v4, v3, v4
	v_ashrrev_i32_e32 v5, 2, v4
	v_lshl_or_b32 v4, v5, 5, v9
	v_cmp_gt_i32_e32 vcc, 16, v4
	v_mov_b32_e32 v103, 0
	s_and_saveexec_b64 s[4:5], vcc
	s_cbranch_execz .LBB0_122
	v_mul_i32_i24_e32 v5, 4, v5
	v_sub_u32_e32 v3, v3, v5
	v_lshrrev_b32_e32 v5, 6, v2
	v_and_b32_e32 v5, 4, v5
	v_lshl_or_b32 v3, v3, 4, v5
	v_or3_b32 v6, v3, v1, v8
	v_ashrrev_i32_e32 v7, 31, v6
	v_lshlrev_b64 v[6:7], 6, v[6:7]
	v_ashrrev_i32_e32 v5, 31, v4
	v_lshl_add_u64 v[6:7], s[12:13], 0, v[6:7]
	v_lshl_add_u64 v[4:5], v[4:5], 2, v[6:7]
	global_load_dword v103, v[4:5], off

.LBB0_124:
	s_andn2_b64 vcc, exec, s[0:1]
	s_cbranch_vccnz .LBB0_135
	s_lshl_b32 s0, s2, 10
	s_cmpk_gt_i32 s0, 0xfff
	s_cbranch_scc1 .LBB0_135
	v_or_b32_e32 v2, s0, v0
	s_waitcnt lgkmcnt(0)
	v_ashrrev_i32_e32 v3, 9, v2
	v_lshrrev_b32_e32 v4, 30, v3
	v_add_u32_e32 v4, v3, v4
	v_bfe_u32 v9, v0, 3, 5
	v_ashrrev_i32_e32 v6, 2, v4
	v_lshlrev_b32_e32 v1, 1, v0
	v_lshl_or_b32 v4, v6, 5, v9
	v_and_b32_e32 v1, 8, v1
	v_and_b32_e32 v8, 3, v0
	v_cmp_gt_i32_e32 vcc, 64, v4
	v_mov_b32_e32 v7, 0
	v_mov_b32_e32 v5, 0
	v_mov_b32_e32 v100, 0
	s_and_saveexec_b64 s[0:1], vcc
	s_cbranch_execz .LBB0_128
	v_mul_i32_i24_e32 v5, 4, v6
	v_sub_u32_e32 v3, v3, v5
	v_lshrrev_b32_e32 v5, 6, v0
	v_and_b32_e32 v5, 4, v5
	v_lshl_or_b32 v3, v3, 4, v5
	v_or3_b32 v10, v3, v1, v8
	v_ashrrev_i32_e32 v11, 31, v10
	v_lshlrev_b64 v[10:11], 8, v[10:11]
	v_ashrrev_i32_e32 v5, 31, v4
	v_lshl_add_u64 v[10:11], s[10:11], 0, v[10:11]
	v_lshl_add_u64 v[4:5], v[4:5], 2, v[10:11]
	global_load_dword v100, v[4:5], off
.LBB0_128:
	s_or_b64 exec, exec, s[0:1]
	s_add_u32 s0, s22, 0x3a000
	s_addc_u32 s1, s23, 0
	v_ashrrev_i32_e32 v3, 31, v2
	v_add_u32_e32 v4, 0x100, v2
	v_lshl_add_u64 v[10:11], v[2:3], 1, s[0:1]
	v_ashrrev_i32_e32 v3, 9, v4
	v_mov_b32_e32 v104, v10
	v_mov_b32_e32 v105, v11
	v_lshrrev_b32_e32 v5, 30, v3
	v_add_u32_e32 v5, v3, v5
	v_ashrrev_i32_e32 v5, 2, v5
	v_lshl_or_b32 v6, v5, 5, v9
	v_cmp_gt_i32_e32 vcc, 64, v6
	v_mov_b32_e32 v101, 0
	s_and_saveexec_b64 s[4:5], vcc
	s_cbranch_execz .LBB0_130
	v_mul_i32_i24_e32 v5, 4, v5
	v_sub_u32_e32 v3, v3, v5
	v_lshrrev_b32_e32 v5, 6, v4
	v_and_b32_e32 v5, 4, v5
	v_lshl_or_b32 v3, v3, 4, v5
	v_or3_b32 v10, v3, v1, v8
	v_ashrrev_i32_e32 v11, 31, v10
	v_lshlrev_b64 v[10:11], 8, v[10:11]
	v_ashrrev_i32_e32 v7, 31, v6
	v_lshl_add_u64 v[10:11], s[10:11], 0, v[10:11]
	v_lshl_add_u64 v[6:7], v[6:7], 2, v[10:11]
	global_load_dword v101, v[6:7], off
.LBB0_130:
	s_or_b64 exec, exec, s[4:5]
	v_ashrrev_i32_e32 v5, 31, v4
	v_lshl_add_u64 v[4:5], v[4:5], 1, s[0:1]
	v_mov_b32_e32 v106, v4
	v_mov_b32_e32 v107, v5
	v_add_u32_e32 v4, 0x200, v2
	v_ashrrev_i32_e32 v3, 9, v4
	v_lshrrev_b32_e32 v5, 30, v3
	v_add_u32_e32 v5, v3, v5
	v_ashrrev_i32_e32 v5, 2, v5
	v_lshl_or_b32 v6, v5, 5, v9
	v_cmp_gt_i32_e32 vcc, 64, v6
	v_mov_b32_e32 v10, 0
	v_mov_b32_e32 v7, 0
	v_mov_b32_e32 v102, 0
	s_and_saveexec_b64 s[4:5], vcc
	s_cbranch_execz .LBB0_132
	v_mul_i32_i24_e32 v5, 4, v5
	v_sub_u32_e32 v3, v3, v5
	v_lshrrev_b32_e32 v5, 6, v0
	v_and_b32_e32 v5, 4, v5
	v_lshl_or_b32 v3, v3, 4, v5
	v_or3_b32 v12, v3, v1, v8
	v_ashrrev_i32_e32 v13, 31, v12
	v_lshlrev_b64 v[12:13], 8, v[12:13]
	v_ashrrev_i32_e32 v7, 31, v6
	v_lshl_add_u64 v[12:13], s[10:11], 0, v[12:13]
	v_lshl_add_u64 v[6:7], v[6:7], 2, v[12:13]
	global_load_dword v102, v[6:7], off
.LBB0_132:
	s_or_b64 exec, exec, s[4:5]
	v_ashrrev_i32_e32 v5, 31, v4
	v_add_u32_e32 v2, 0x300, v2
	v_lshl_add_u64 v[4:5], v[4:5], 1, s[0:1]
	v_ashrrev_i32_e32 v3, 9, v2
	v_mov_b32_e32 v108, v4
	v_mov_b32_e32 v109, v5
	v_lshrrev_b32_e32 v4, 30, v3
	v_add_u32_e32 v4, v3, v4
	v_ashrrev_i32_e32 v5, 2, v4
	v_lshl_or_b32 v4, v5, 5, v9
	v_cmp_gt_i32_e32 vcc, 64, v4
	v_mov_b32_e32 v103, 0
	s_and_saveexec_b64 s[4:5], vcc
	s_cbranch_execz .LBB0_134
	v_mul_i32_i24_e32 v5, 4, v5
	v_sub_u32_e32 v3, v3, v5
	v_lshrrev_b32_e32 v5, 6, v2
	v_and_b32_e32 v5, 4, v5
	v_lshl_or_b32 v3, v3, 4, v5
	v_or3_b32 v6, v3, v1, v8
	v_ashrrev_i32_e32 v7, 31, v6
	v_lshlrev_b64 v[6:7], 8, v[6:7]
	v_ashrrev_i32_e32 v5, 31, v4
	v_lshl_add_u64 v[6:7], s[10:11], 0, v[6:7]
	v_lshl_add_u64 v[4:5], v[4:5], 2, v[6:7]
	global_load_dword v103, v[4:5], off

.LBB0_136:
	s_and_b64 vcc, exec, s[4:5]
	s_cbranch_vccz .LBB0_147
	s_lshl_b32 s6, s2, 10
	s_cmpk_gt_i32 s6, 0xfff
	s_cbranch_scc1 .LBB0_147
	v_or_b32_e32 v2, s6, v0
	s_waitcnt lgkmcnt(0)
	v_ashrrev_i32_e32 v3, 9, v2
	s_lshl_b32 s0, s3, 12
	v_lshrrev_b32_e32 v4, 30, v3
	s_add_i32 s4, s0, 0xffff1000
	s_mov_b32 s5, 0
	v_add_u32_e32 v4, v3, v4
	s_lshl_b64 s[0:1], s[4:5], 2
	v_bfe_u32 v9, v0, 3, 5
	v_ashrrev_i32_e32 v5, 2, v4
	s_add_u32 s0, s50, s0
	v_lshlrev_b32_e32 v1, 1, v0
	v_lshl_or_b32 v4, v5, 5, v9
	s_addc_u32 s1, s51, s1
	v_and_b32_e32 v1, 8, v1
	v_and_b32_e32 v8, 3, v0
	v_cmp_gt_i32_e32 vcc, 64, v4
	v_mov_b32_e32 v7, 0
	v_mov_b32_e32 v6, 0
	v_mov_b32_e32 v100, 0
	s_and_saveexec_b64 s[6:7], vcc
	s_cbranch_execz .LBB0_140
	v_mul_i32_i24_e32 v5, 4, v5
	v_sub_u32_e32 v3, v3, v5
	v_lshrrev_b32_e32 v5, 6, v0
	v_and_b32_e32 v5, 4, v5
	v_lshl_or_b32 v3, v3, 4, v5
	v_or3_b32 v10, v3, v1, v8
	v_ashrrev_i32_e32 v11, 31, v10
	v_lshlrev_b64 v[10:11], 8, v[10:11]
	v_ashrrev_i32_e32 v5, 31, v4
	v_lshl_add_u64 v[10:11], s[0:1], 0, v[10:11]
	v_lshl_add_u64 v[4:5], v[4:5], 2, v[10:11]
	global_load_dword v100, v[4:5], off
.LBB0_140:
	s_or_b64 exec, exec, s[6:7]
	s_lshl_b64 s[4:5], s[4:5], 1
	s_add_u32 s4, s22, s4
	s_addc_u32 s5, s23, s5
	v_ashrrev_i32_e32 v3, 31, v2
	v_lshl_add_u64 v[10:11], v[2:3], 1, s[4:5]
	s_mov_b64 s[4:5], 0x36000
	v_lshl_add_u64 v[4:5], v[10:11], 0, s[4:5]
	v_add_co_u32_e32 v10, vcc, 0x36000, v10
	v_add_u32_e32 v3, 0x100, v2
	s_nop 0
	v_addc_co_u32_e32 v11, vcc, 0, v11, vcc
	v_mov_b32_e32 v104, v10
	v_mov_b32_e32 v105, v11
	v_ashrrev_i32_e32 v10, 9, v3
	v_lshrrev_b32_e32 v6, 30, v10
	v_add_u32_e32 v6, v10, v6
	v_ashrrev_i32_e32 v11, 2, v6
	v_lshl_or_b32 v6, v11, 5, v9
	v_cmp_gt_i32_e32 vcc, 64, v6
	v_mov_b32_e32 v101, 0
	s_and_saveexec_b64 s[4:5], vcc
	s_cbranch_execz .LBB0_142
	v_mul_i32_i24_e32 v7, 4, v11
	v_lshrrev_b32_e32 v3, 6, v3
	v_sub_u32_e32 v7, v10, v7
	v_and_b32_e32 v3, 4, v3
	v_lshl_or_b32 v3, v7, 4, v3
	v_or3_b32 v10, v3, v1, v8
	v_ashrrev_i32_e32 v11, 31, v10
	v_lshlrev_b64 v[10:11], 8, v[10:11]
	v_ashrrev_i32_e32 v7, 31, v6
	v_lshl_add_u64 v[10:11], s[0:1], 0, v[10:11]
	v_lshl_add_u64 v[6:7], v[6:7], 2, v[10:11]
	global_load_dword v101, v[6:7], off
.LBB0_142:
	s_or_b64 exec, exec, s[4:5]
	v_add_u32_e32 v3, 0x200, v2
	v_mov_b32_e32 v106, v4
	v_mov_b32_e32 v107, v5
	v_ashrrev_i32_e32 v7, 9, v3
	v_lshrrev_b32_e32 v3, 30, v7
	v_add_u32_e32 v3, v7, v3
	v_ashrrev_i32_e32 v10, 2, v3
	v_lshl_or_b32 v6, v10, 5, v9
	v_cmp_gt_i32_e32 vcc, 64, v6
	v_mov_b32_e32 v3, 0
	v_mov_b32_e32 v11, 0
	v_mov_b32_e32 v102, 0
	s_and_saveexec_b64 s[4:5], vcc
	s_cbranch_execz .LBB0_144
	v_mul_i32_i24_e32 v10, 4, v10
	v_sub_u32_e32 v7, v7, v10
	v_lshrrev_b32_e32 v10, 6, v0
	v_and_b32_e32 v10, 4, v10
	v_lshl_or_b32 v7, v7, 4, v10
	v_or3_b32 v10, v7, v1, v8
	v_ashrrev_i32_e32 v11, 31, v10
	v_lshlrev_b64 v[10:11], 8, v[10:11]
	v_ashrrev_i32_e32 v7, 31, v6
	v_lshl_add_u64 v[10:11], s[0:1], 0, v[10:11]
	v_lshl_add_u64 v[6:7], v[6:7], 2, v[10:11]
	global_load_dword v102, v[6:7], off
.LBB0_144:
	s_or_b64 exec, exec, s[4:5]
	v_add_u32_e32 v6, 0x300, v2
	v_ashrrev_i32_e32 v7, 9, v6
	v_lshrrev_b32_e32 v2, 30, v7
	v_add_u32_e32 v2, v7, v2
	v_ashrrev_i32_e32 v10, 2, v2
	v_lshl_or_b32 v2, v10, 5, v9
	v_cmp_gt_i32_e32 vcc, 64, v2
	v_mov_b32_e32 v108, v4
	v_mov_b32_e32 v109, v5
	v_mov_b32_e32 v103, 0
	s_and_saveexec_b64 s[4:5], vcc
	s_cbranch_execz .LBB0_146
	v_mul_i32_i24_e32 v3, 4, v10
	v_lshrrev_b32_e32 v6, 6, v6
	v_sub_u32_e32 v3, v7, v3
	v_and_b32_e32 v6, 4, v6
	v_lshl_or_b32 v3, v3, 4, v6
	v_or3_b32 v6, v3, v1, v8
	v_ashrrev_i32_e32 v7, 31, v6
	v_lshlrev_b64 v[6:7], 8, v[6:7]
	v_ashrrev_i32_e32 v3, 31, v2
	v_lshl_add_u64 v[6:7], s[0:1], 0, v[6:7]
	v_lshl_add_u64 v[2:3], v[2:3], 2, v[6:7]
	global_load_dword v103, v[2:3], off

.LBB0_148:
	s_andn2_b64 vcc, exec, s[4:5]
	s_cbranch_vccnz .LBB0_159
	s_lshl_b32 s6, s2, 10
	s_cmpk_gt_i32 s6, 0xfff
	s_cbranch_scc1 .LBB0_159
	s_lshl_b32 s0, s3, 12
	s_add_i32 s4, s0, 0xffff4000
	s_mov_b32 s5, 0
	v_or_b32_e32 v2, s6, v0
	s_waitcnt lgkmcnt(0)
	v_lshlrev_b32_e32 v3, 1, v0
	s_lshl_b64 s[0:1], s[4:5], 2
	v_and_b32_e32 v8, 8, v3
	v_ashrrev_i32_e32 v3, 9, v2
	s_add_u32 s0, s48, s0
	v_lshrrev_b32_e32 v4, 30, v3
	s_addc_u32 s1, s49, s1
	v_add_u32_e32 v4, v3, v4
	s_cmp_eq_u32 s3, 12
	v_bfe_u32 v10, v0, 3, 5
	v_ashrrev_i32_e32 v5, 2, v4
	v_mov_b32_e32 v1, 0x3e38aa3b
	s_cselect_b64 vcc, -1, 0
	v_lshl_or_b32 v4, v5, 5, v10
	v_cndmask_b32_e32 v1, 1.0, v1, vcc
	v_and_b32_e32 v9, 3, v0
	v_cmp_gt_i32_e32 vcc, 64, v4
	v_mov_b32_e32 v7, 0
	v_mov_b32_e32 v6, 0
	v_mov_b32_e32 v100, 0
	s_and_saveexec_b64 s[6:7], vcc
	s_cbranch_execz .LBB0_152
	v_mul_i32_i24_e32 v5, 4, v5
	v_sub_u32_e32 v3, v3, v5
	v_lshrrev_b32_e32 v5, 6, v0
	v_and_b32_e32 v5, 4, v5
	v_lshl_or_b32 v3, v3, 4, v5
	v_or3_b32 v12, v3, v8, v9
	v_ashrrev_i32_e32 v13, 31, v12
	v_lshlrev_b64 v[12:13], 8, v[12:13]
	v_ashrrev_i32_e32 v5, 31, v4
	v_lshl_add_u64 v[12:13], s[0:1], 0, v[12:13]
	v_lshl_add_u64 v[4:5], v[4:5], 2, v[12:13]
	global_load_dword v100, v[4:5], off
.LBB0_152:
	s_or_b64 exec, exec, s[6:7]
	s_lshl_b64 s[4:5], s[4:5], 1
	s_add_u32 s4, s22, s4
	s_addc_u32 s5, s23, s5
	v_ashrrev_i32_e32 v3, 31, v2
	v_lshl_add_u64 v[12:13], v[2:3], 1, s[4:5]
	s_mov_b64 s[4:5], 0x30000
	v_lshl_add_u64 v[4:5], v[12:13], 0, s[4:5]
	v_add_co_u32_e32 v12, vcc, 0x30000, v12
	v_add_u32_e32 v3, 0x100, v2
	s_nop 0
	v_addc_co_u32_e32 v13, vcc, 0, v13, vcc
	v_ashrrev_i32_e32 v11, 9, v3
	v_mov_b32_e32 v112, v1
	v_mov_b32_e32 v104, v12
	v_mov_b32_e32 v105, v13
	v_lshrrev_b32_e32 v6, 30, v11
	v_add_u32_e32 v6, v11, v6
	v_ashrrev_i32_e32 v12, 2, v6
	v_lshl_or_b32 v6, v12, 5, v10
	v_cmp_gt_i32_e32 vcc, 64, v6
	v_mov_b32_e32 v101, 0
	s_and_saveexec_b64 s[4:5], vcc
	s_cbranch_execz .LBB0_154
	v_mul_i32_i24_e32 v7, 4, v12
	v_lshrrev_b32_e32 v3, 6, v3
	v_sub_u32_e32 v7, v11, v7
	v_and_b32_e32 v3, 4, v3
	v_lshl_or_b32 v3, v7, 4, v3
	v_or3_b32 v12, v3, v8, v9
	v_ashrrev_i32_e32 v13, 31, v12
	v_lshlrev_b64 v[12:13], 8, v[12:13]
	v_ashrrev_i32_e32 v7, 31, v6
	v_lshl_add_u64 v[12:13], s[0:1], 0, v[12:13]
	v_lshl_add_u64 v[6:7], v[6:7], 2, v[12:13]
	global_load_dword v101, v[6:7], off
.LBB0_154:
	s_or_b64 exec, exec, s[4:5]
	v_add_u32_e32 v3, 0x200, v2
	v_mov_b32_e32 v106, v4
	v_mov_b32_e32 v107, v5
	v_ashrrev_i32_e32 v7, 9, v3
	v_lshrrev_b32_e32 v3, 30, v7
	v_add_u32_e32 v3, v7, v3
	v_ashrrev_i32_e32 v11, 2, v3
	v_lshl_or_b32 v6, v11, 5, v10
	v_cmp_gt_i32_e32 vcc, 64, v6
	v_mov_b32_e32 v3, 0
	v_mov_b32_e32 v12, 0
	v_mov_b32_e32 v102, 0
	s_and_saveexec_b64 s[4:5], vcc
	s_cbranch_execz .LBB0_156
	v_mul_i32_i24_e32 v11, 4, v11
	v_sub_u32_e32 v7, v7, v11
	v_lshrrev_b32_e32 v11, 6, v0
	v_and_b32_e32 v11, 4, v11
	v_lshl_or_b32 v7, v7, 4, v11
	v_or3_b32 v12, v7, v8, v9
	v_ashrrev_i32_e32 v13, 31, v12
	v_lshlrev_b64 v[12:13], 8, v[12:13]
	v_ashrrev_i32_e32 v7, 31, v6
	v_lshl_add_u64 v[12:13], s[0:1], 0, v[12:13]
	v_lshl_add_u64 v[6:7], v[6:7], 2, v[12:13]
	global_load_dword v102, v[6:7], off
.LBB0_156:
	s_or_b64 exec, exec, s[4:5]
	v_add_u32_e32 v6, 0x300, v2
	v_ashrrev_i32_e32 v7, 9, v6
	v_lshrrev_b32_e32 v2, 30, v7
	v_add_u32_e32 v2, v7, v2
	v_ashrrev_i32_e32 v11, 2, v2
	v_lshl_or_b32 v2, v11, 5, v10
	v_cmp_gt_i32_e32 vcc, 64, v2
	v_mov_b32_e32 v108, v4
	v_mov_b32_e32 v109, v5
	v_mov_b32_e32 v103, 0
	s_and_saveexec_b64 s[4:5], vcc
	s_cbranch_execz .LBB0_158
	v_mul_i32_i24_e32 v3, 4, v11
	v_lshrrev_b32_e32 v6, 6, v6
	v_sub_u32_e32 v3, v7, v3
	v_and_b32_e32 v6, 4, v6
	v_lshl_or_b32 v3, v3, 4, v6
	v_or3_b32 v6, v3, v8, v9
	v_ashrrev_i32_e32 v7, 31, v6
	v_lshlrev_b64 v[6:7], 8, v[6:7]
	v_ashrrev_i32_e32 v3, 31, v2
	v_lshl_add_u64 v[6:7], s[0:1], 0, v[6:7]
	v_lshl_add_u64 v[2:3], v[2:3], 2, v[6:7]
	global_load_dword v103, v[2:3], off
.LBB0_158:
	s_or_b64 exec, exec, s[4:5]
	s_waitcnt vmcnt(0)
	v_fma_mixlo_f16 v100, v112, v100, 0
	v_fma_mixlo_f16 v101, v112, v101, 0
	v_fma_mixlo_f16 v102, v112, v102, 0
	v_fma_mixlo_f16 v103, v112, v103, 0
	global_store_short v[104:105], v100, off
	global_store_short v[106:107], v101, off offset:512
	global_store_short v[108:109], v102, off offset:1024
	global_store_short v[4:5], v103, off offset:1536

.LBB0_160:
	s_andn2_b64 vcc, exec, s[4:5]
	s_cbranch_vccnz .LBB0_171
	s_lshl_b32 s0, s2, 10
	s_cmpk_gt_i32 s0, 0x3fff
	s_cbranch_scc1 .LBB0_171
	v_or_b32_e32 v2, s0, v0
	s_waitcnt lgkmcnt(0)
	v_ashrrev_i32_e32 v3, 9, v2
	v_lshrrev_b32_e32 v4, 28, v3
	v_add_u32_e32 v4, v3, v4
	v_bfe_u32 v9, v0, 3, 5
	v_ashrrev_i32_e32 v6, 4, v4
	v_lshlrev_b32_e32 v1, 1, v0
	v_lshl_or_b32 v4, v6, 5, v9
	v_and_b32_e32 v1, 8, v1
	v_and_b32_e32 v8, 3, v0
	v_cmp_gt_i32_e32 vcc, 64, v4
	v_mov_b32_e32 v7, 0
	v_mov_b32_e32 v5, 0
	v_mov_b32_e32 v100, 0
	s_and_saveexec_b64 s[0:1], vcc
	s_cbranch_execz .LBB0_164
	v_mul_i32_i24_e32 v5, 16, v6
	v_sub_u32_e32 v3, v3, v5
	v_lshrrev_b32_e32 v5, 6, v0
	v_and_b32_e32 v5, 4, v5
	v_lshl_or_b32 v3, v3, 4, v5
	v_or3_b32 v10, v3, v1, v8
	v_ashrrev_i32_e32 v11, 31, v10
	v_lshlrev_b64 v[10:11], 8, v[10:11]
	v_ashrrev_i32_e32 v5, 31, v4
	v_lshl_add_u64 v[10:11], s[46:47], 0, v[10:11]
	v_lshl_add_u64 v[4:5], v[4:5], 2, v[10:11]
	global_load_dword v100, v[4:5], off
.LBB0_164:
	s_or_b64 exec, exec, s[0:1]
	s_add_u32 s0, s22, 0x28000
	s_addc_u32 s1, s23, 0
	v_ashrrev_i32_e32 v3, 31, v2
	v_add_u32_e32 v4, 0x100, v2
	v_lshl_add_u64 v[10:11], v[2:3], 1, s[0:1]
	v_ashrrev_i32_e32 v3, 9, v4
	v_mov_b32_e32 v104, v10
	v_mov_b32_e32 v105, v11
	v_lshrrev_b32_e32 v5, 28, v3
	v_add_u32_e32 v5, v3, v5
	v_ashrrev_i32_e32 v5, 4, v5
	v_lshl_or_b32 v6, v5, 5, v9
	v_cmp_gt_i32_e32 vcc, 64, v6
	v_mov_b32_e32 v101, 0
	s_and_saveexec_b64 s[4:5], vcc
	s_cbranch_execz .LBB0_166
	v_mul_i32_i24_e32 v5, 16, v5
	v_sub_u32_e32 v3, v3, v5
	v_lshrrev_b32_e32 v5, 6, v4
	v_and_b32_e32 v5, 4, v5
	v_lshl_or_b32 v3, v3, 4, v5
	v_or3_b32 v10, v3, v1, v8
	v_ashrrev_i32_e32 v11, 31, v10
	v_lshlrev_b64 v[10:11], 8, v[10:11]
	v_ashrrev_i32_e32 v7, 31, v6
	v_lshl_add_u64 v[10:11], s[46:47], 0, v[10:11]
	v_lshl_add_u64 v[6:7], v[6:7], 2, v[10:11]
	global_load_dword v101, v[6:7], off
.LBB0_166:
	s_or_b64 exec, exec, s[4:5]
	v_ashrrev_i32_e32 v5, 31, v4
	v_lshl_add_u64 v[4:5], v[4:5], 1, s[0:1]
	v_mov_b32_e32 v106, v4
	v_mov_b32_e32 v107, v5
	v_add_u32_e32 v4, 0x200, v2
	v_ashrrev_i32_e32 v3, 9, v4
	v_lshrrev_b32_e32 v5, 28, v3
	v_add_u32_e32 v5, v3, v5
	v_ashrrev_i32_e32 v5, 4, v5
	v_lshl_or_b32 v6, v5, 5, v9
	v_cmp_gt_i32_e32 vcc, 64, v6
	v_mov_b32_e32 v10, 0
	v_mov_b32_e32 v7, 0
	v_mov_b32_e32 v102, 0
	s_and_saveexec_b64 s[4:5], vcc
	s_cbranch_execz .LBB0_168
	v_mul_i32_i24_e32 v5, 16, v5
	v_sub_u32_e32 v3, v3, v5
	v_lshrrev_b32_e32 v5, 6, v0
	v_and_b32_e32 v5, 4, v5
	v_lshl_or_b32 v3, v3, 4, v5
	v_or3_b32 v12, v3, v1, v8
	v_ashrrev_i32_e32 v13, 31, v12
	v_lshlrev_b64 v[12:13], 8, v[12:13]
	v_ashrrev_i32_e32 v7, 31, v6
	v_lshl_add_u64 v[12:13], s[46:47], 0, v[12:13]
	v_lshl_add_u64 v[6:7], v[6:7], 2, v[12:13]
	global_load_dword v102, v[6:7], off
.LBB0_168:
	s_or_b64 exec, exec, s[4:5]
	v_ashrrev_i32_e32 v5, 31, v4
	v_add_u32_e32 v2, 0x300, v2
	v_lshl_add_u64 v[4:5], v[4:5], 1, s[0:1]
	v_ashrrev_i32_e32 v3, 9, v2
	v_mov_b32_e32 v108, v4
	v_mov_b32_e32 v109, v5
	v_lshrrev_b32_e32 v4, 28, v3
	v_add_u32_e32 v4, v3, v4
	v_ashrrev_i32_e32 v5, 4, v4
	v_lshl_or_b32 v4, v5, 5, v9
	v_cmp_gt_i32_e32 vcc, 64, v4
	v_mov_b32_e32 v103, 0
	s_and_saveexec_b64 s[4:5], vcc
	s_cbranch_execz .LBB0_170
	v_mul_i32_i24_e32 v5, 16, v5
	v_sub_u32_e32 v3, v3, v5
	v_lshrrev_b32_e32 v5, 6, v2
	v_and_b32_e32 v5, 4, v5
	v_lshl_or_b32 v3, v3, 4, v5
	v_or3_b32 v6, v3, v1, v8
	v_ashrrev_i32_e32 v7, 31, v6
	v_lshlrev_b64 v[6:7], 8, v[6:7]
	v_ashrrev_i32_e32 v5, 31, v4
	v_lshl_add_u64 v[6:7], s[46:47], 0, v[6:7]
	v_lshl_add_u64 v[4:5], v[4:5], 2, v[6:7]
	global_load_dword v103, v[4:5], off

.LBB0_172:
	s_andn2_b64 vcc, exec, s[4:5]
	s_cbranch_vccnz .LBB0_183
	s_lshl_b32 s0, s2, 10
	s_cmpk_gt_i32 s0, 0x3fff
	s_cbranch_scc1 .LBB0_183
	v_or_b32_e32 v2, s0, v0
	s_waitcnt lgkmcnt(0)
	v_ashrrev_i32_e32 v3, 9, v2
	v_lshrrev_b32_e32 v4, 30, v3
	v_add_u32_e32 v4, v3, v4
	v_bfe_u32 v9, v0, 3, 5
	v_ashrrev_i32_e32 v6, 2, v4
	v_lshlrev_b32_e32 v1, 1, v0
	v_lshl_or_b32 v4, v6, 5, v9
	s_movk_i32 s4, 0x100
	v_and_b32_e32 v1, 8, v1
	v_and_b32_e32 v8, 3, v0
	v_cmp_gt_i32_e32 vcc, s4, v4
	v_mov_b32_e32 v7, 0
	v_mov_b32_e32 v5, 0
	v_mov_b32_e32 v100, 0
	s_and_saveexec_b64 s[0:1], vcc
	s_cbranch_execz .LBB0_176
	v_mul_i32_i24_e32 v5, 4, v6
	v_sub_u32_e32 v3, v3, v5
	v_lshrrev_b32_e32 v5, 6, v0
	v_and_b32_e32 v5, 4, v5
	v_lshl_or_b32 v3, v3, 4, v5
	v_or3_b32 v10, v3, v1, v8
	v_ashrrev_i32_e32 v11, 31, v10
	v_lshlrev_b64 v[10:11], 10, v[10:11]
	v_ashrrev_i32_e32 v5, 31, v4
	v_lshl_add_u64 v[10:11], s[44:45], 0, v[10:11]
	v_lshl_add_u64 v[4:5], v[4:5], 2, v[10:11]
	global_load_dword v100, v[4:5], off
.LBB0_176:
	s_or_b64 exec, exec, s[0:1]
	s_add_u32 s0, s22, 0x20000
	s_addc_u32 s1, s23, 0
	v_ashrrev_i32_e32 v3, 31, v2
	v_add_u32_e32 v4, 0x100, v2
	v_lshl_add_u64 v[10:11], v[2:3], 1, s[0:1]
	v_ashrrev_i32_e32 v3, 9, v4
	v_mov_b32_e32 v104, v10
	v_mov_b32_e32 v105, v11
	v_lshrrev_b32_e32 v5, 30, v3
	v_add_u32_e32 v5, v3, v5
	v_ashrrev_i32_e32 v5, 2, v5
	v_lshl_or_b32 v6, v5, 5, v9
	v_cmp_gt_i32_e32 vcc, s4, v6
	v_mov_b32_e32 v101, 0
	s_and_saveexec_b64 s[4:5], vcc
	s_cbranch_execz .LBB0_178
	v_mul_i32_i24_e32 v5, 4, v5
	v_sub_u32_e32 v3, v3, v5
	v_lshrrev_b32_e32 v5, 6, v4
	v_and_b32_e32 v5, 4, v5
	v_lshl_or_b32 v3, v3, 4, v5
	v_or3_b32 v10, v3, v1, v8
	v_ashrrev_i32_e32 v11, 31, v10
	v_lshlrev_b64 v[10:11], 10, v[10:11]
	v_ashrrev_i32_e32 v7, 31, v6
	v_lshl_add_u64 v[10:11], s[44:45], 0, v[10:11]
	v_lshl_add_u64 v[6:7], v[6:7], 2, v[10:11]
	global_load_dword v101, v[6:7], off
.LBB0_178:
	s_or_b64 exec, exec, s[4:5]
	v_ashrrev_i32_e32 v5, 31, v4
	v_lshl_add_u64 v[4:5], v[4:5], 1, s[0:1]
	v_mov_b32_e32 v106, v4
	v_mov_b32_e32 v107, v5
	v_add_u32_e32 v4, 0x200, v2
	v_ashrrev_i32_e32 v3, 9, v4
	v_lshrrev_b32_e32 v5, 30, v3
	v_add_u32_e32 v5, v3, v5
	v_ashrrev_i32_e32 v5, 2, v5
	v_lshl_or_b32 v6, v5, 5, v9
	s_movk_i32 s6, 0x100
	v_cmp_gt_i32_e32 vcc, s6, v6
	v_mov_b32_e32 v10, 0
	v_mov_b32_e32 v7, 0
	v_mov_b32_e32 v102, 0
	s_and_saveexec_b64 s[4:5], vcc
	s_cbranch_execz .LBB0_180
	v_mul_i32_i24_e32 v5, 4, v5
	v_sub_u32_e32 v3, v3, v5
	v_lshrrev_b32_e32 v5, 6, v0
	v_and_b32_e32 v5, 4, v5
	v_lshl_or_b32 v3, v3, 4, v5
	v_or3_b32 v12, v3, v1, v8
	v_ashrrev_i32_e32 v13, 31, v12
	v_lshlrev_b64 v[12:13], 10, v[12:13]
	v_ashrrev_i32_e32 v7, 31, v6
	v_lshl_add_u64 v[12:13], s[44:45], 0, v[12:13]
	v_lshl_add_u64 v[6:7], v[6:7], 2, v[12:13]
	global_load_dword v102, v[6:7], off
.LBB0_180:
	s_or_b64 exec, exec, s[4:5]
	v_ashrrev_i32_e32 v5, 31, v4
	v_add_u32_e32 v2, 0x300, v2
	v_lshl_add_u64 v[4:5], v[4:5], 1, s[0:1]
	v_ashrrev_i32_e32 v3, 9, v2
	v_mov_b32_e32 v108, v4
	v_mov_b32_e32 v109, v5
	v_lshrrev_b32_e32 v4, 30, v3
	v_add_u32_e32 v4, v3, v4
	v_ashrrev_i32_e32 v5, 2, v4
	v_lshl_or_b32 v4, v5, 5, v9
	v_cmp_gt_i32_e32 vcc, s6, v4
	v_mov_b32_e32 v103, 0
	s_and_saveexec_b64 s[4:5], vcc
	s_cbranch_execz .LBB0_182
	v_mul_i32_i24_e32 v5, 4, v5
	v_sub_u32_e32 v3, v3, v5
	v_lshrrev_b32_e32 v5, 6, v2
	v_and_b32_e32 v5, 4, v5
	v_lshl_or_b32 v3, v3, 4, v5
	v_or3_b32 v6, v3, v1, v8
	v_ashrrev_i32_e32 v7, 31, v6
	v_lshlrev_b64 v[6:7], 10, v[6:7]
	v_ashrrev_i32_e32 v5, 31, v4
	v_lshl_add_u64 v[6:7], s[44:45], 0, v[6:7]
	v_lshl_add_u64 v[4:5], v[4:5], 2, v[6:7]
	global_load_dword v103, v[4:5], off

.LBB0_184:
	s_and_b64 vcc, exec, s[4:5]
	s_cbranch_vccz .LBB0_195
	s_lshl_b32 s6, s2, 10
	s_cmpk_gt_i32 s6, 0xfff
	s_cbranch_scc1 .LBB0_195
	s_lshl_b32 s0, s3, 12
	s_add_i32 s4, s0, 0xffffa000
	s_mov_b32 s5, 0
	v_or_b32_e32 v2, s6, v0
	s_waitcnt lgkmcnt(0)
	v_lshlrev_b32_e32 v3, 1, v0
	s_lshl_b64 s[0:1], s[4:5], 2
	v_and_b32_e32 v8, 8, v3
	v_ashrrev_i32_e32 v3, 9, v2
	s_add_u32 s0, s42, s0
	v_lshrrev_b32_e32 v4, 30, v3
	s_addc_u32 s1, s43, s1
	v_add_u32_e32 v4, v3, v4
	s_cmp_eq_u32 s3, 6
	v_bfe_u32 v10, v0, 3, 5
	v_ashrrev_i32_e32 v5, 2, v4
	v_mov_b32_e32 v1, 0x3eb8aa3b
	s_cselect_b64 vcc, -1, 0
	v_lshl_or_b32 v4, v5, 5, v10
	v_cndmask_b32_e32 v1, 1.0, v1, vcc
	v_and_b32_e32 v9, 3, v0
	v_cmp_gt_i32_e32 vcc, 64, v4
	v_mov_b32_e32 v7, 0
	v_mov_b32_e32 v6, 0
	v_mov_b32_e32 v100, 0
	s_and_saveexec_b64 s[6:7], vcc
	s_cbranch_execz .LBB0_188
	v_mul_i32_i24_e32 v5, 4, v5
	v_sub_u32_e32 v3, v3, v5
	v_lshrrev_b32_e32 v5, 6, v0
	v_and_b32_e32 v5, 4, v5
	v_lshl_or_b32 v3, v3, 4, v5
	v_or3_b32 v12, v3, v8, v9
	v_ashrrev_i32_e32 v13, 31, v12
	v_lshlrev_b64 v[12:13], 8, v[12:13]
	v_ashrrev_i32_e32 v5, 31, v4
	v_lshl_add_u64 v[12:13], s[0:1], 0, v[12:13]
	v_lshl_add_u64 v[4:5], v[4:5], 2, v[12:13]
	global_load_dword v100, v[4:5], off
.LBB0_188:
	s_or_b64 exec, exec, s[6:7]
	s_lshl_b64 s[4:5], s[4:5], 1
	s_add_u32 s4, s22, s4
	s_addc_u32 s5, s23, s5
	v_ashrrev_i32_e32 v3, 31, v2
	v_lshl_add_u64 v[12:13], v[2:3], 1, s[4:5]
	s_mov_b64 s[4:5], 0x18000
	v_lshl_add_u64 v[4:5], v[12:13], 0, s[4:5]
	v_add_co_u32_e32 v12, vcc, 0x18000, v12
	v_add_u32_e32 v3, 0x100, v2
	s_nop 0
	v_addc_co_u32_e32 v13, vcc, 0, v13, vcc
	v_ashrrev_i32_e32 v11, 9, v3
	v_mov_b32_e32 v112, v1
	v_mov_b32_e32 v104, v12
	v_mov_b32_e32 v105, v13
	v_lshrrev_b32_e32 v6, 30, v11
	v_add_u32_e32 v6, v11, v6
	v_ashrrev_i32_e32 v12, 2, v6
	v_lshl_or_b32 v6, v12, 5, v10
	v_cmp_gt_i32_e32 vcc, 64, v6
	v_mov_b32_e32 v101, 0
	s_and_saveexec_b64 s[4:5], vcc
	s_cbranch_execz .LBB0_190
	v_mul_i32_i24_e32 v7, 4, v12
	v_lshrrev_b32_e32 v3, 6, v3
	v_sub_u32_e32 v7, v11, v7
	v_and_b32_e32 v3, 4, v3
	v_lshl_or_b32 v3, v7, 4, v3
	v_or3_b32 v12, v3, v8, v9
	v_ashrrev_i32_e32 v13, 31, v12
	v_lshlrev_b64 v[12:13], 8, v[12:13]
	v_ashrrev_i32_e32 v7, 31, v6
	v_lshl_add_u64 v[12:13], s[0:1], 0, v[12:13]
	v_lshl_add_u64 v[6:7], v[6:7], 2, v[12:13]
	global_load_dword v101, v[6:7], off

.LBB0_196:
	s_andn2_b64 vcc, exec, s[4:5]
	s_cbranch_vccnz .LBB0_207
	s_lshl_b32 s0, s2, 10
	s_cmpk_gt_i32 s0, 0x3fff
	s_cbranch_scc1 .LBB0_207
	v_or_b32_e32 v2, s0, v0
	s_waitcnt lgkmcnt(0)
	v_ashrrev_i32_e32 v3, 9, v2
	v_lshrrev_b32_e32 v4, 28, v3
	v_add_u32_e32 v4, v3, v4
	v_bfe_u32 v9, v0, 3, 5
	v_ashrrev_i32_e32 v6, 4, v4
	v_lshlrev_b32_e32 v1, 1, v0
	v_lshl_or_b32 v4, v6, 5, v9
	v_and_b32_e32 v1, 8, v1
	v_and_b32_e32 v8, 3, v0
	v_cmp_gt_i32_e32 vcc, 64, v4
	v_mov_b32_e32 v7, 0
	v_mov_b32_e32 v5, 0
	v_mov_b32_e32 v100, 0
	s_and_saveexec_b64 s[0:1], vcc
	s_cbranch_execz .LBB0_200
	v_mul_i32_i24_e32 v5, 16, v6
	v_sub_u32_e32 v3, v3, v5
	v_lshrrev_b32_e32 v5, 6, v0
	v_and_b32_e32 v5, 4, v5
	v_lshl_or_b32 v3, v3, 4, v5
	v_or3_b32 v10, v3, v1, v8
	v_ashrrev_i32_e32 v11, 31, v10
	v_lshlrev_b64 v[10:11], 8, v[10:11]
	v_ashrrev_i32_e32 v5, 31, v4
	v_lshl_add_u64 v[10:11], s[40:41], 0, v[10:11]
	v_lshl_add_u64 v[4:5], v[4:5], 2, v[10:11]
	global_load_dword v100, v[4:5], off
.LBB0_200:
	s_or_b64 exec, exec, s[0:1]
	s_add_u32 s0, s22, 0x10000
	s_addc_u32 s1, s23, 0
	v_ashrrev_i32_e32 v3, 31, v2
	v_add_u32_e32 v4, 0x100, v2
	v_lshl_add_u64 v[10:11], v[2:3], 1, s[0:1]
	v_ashrrev_i32_e32 v3, 9, v4
	v_mov_b32_e32 v104, v10
	v_mov_b32_e32 v105, v11
	v_lshrrev_b32_e32 v5, 28, v3
	v_add_u32_e32 v5, v3, v5
	v_ashrrev_i32_e32 v5, 4, v5
	v_lshl_or_b32 v6, v5, 5, v9
	v_cmp_gt_i32_e32 vcc, 64, v6
	v_mov_b32_e32 v101, 0
	s_and_saveexec_b64 s[4:5], vcc
	s_cbranch_execz .LBB0_202
	v_mul_i32_i24_e32 v5, 16, v5
	v_sub_u32_e32 v3, v3, v5
	v_lshrrev_b32_e32 v5, 6, v4
	v_and_b32_e32 v5, 4, v5
	v_lshl_or_b32 v3, v3, 4, v5
	v_or3_b32 v10, v3, v1, v8
	v_ashrrev_i32_e32 v11, 31, v10
	v_lshlrev_b64 v[10:11], 8, v[10:11]
	v_ashrrev_i32_e32 v7, 31, v6
	v_lshl_add_u64 v[10:11], s[40:41], 0, v[10:11]
	v_lshl_add_u64 v[6:7], v[6:7], 2, v[10:11]
	global_load_dword v101, v[6:7], off
.LBB0_202:
	s_or_b64 exec, exec, s[4:5]
	v_ashrrev_i32_e32 v5, 31, v4
	v_lshl_add_u64 v[4:5], v[4:5], 1, s[0:1]
	v_mov_b32_e32 v106, v4
	v_mov_b32_e32 v107, v5
	v_add_u32_e32 v4, 0x200, v2
	v_ashrrev_i32_e32 v3, 9, v4
	v_lshrrev_b32_e32 v5, 28, v3
	v_add_u32_e32 v5, v3, v5
	v_ashrrev_i32_e32 v5, 4, v5
	v_lshl_or_b32 v6, v5, 5, v9
	v_cmp_gt_i32_e32 vcc, 64, v6
	v_mov_b32_e32 v10, 0
	v_mov_b32_e32 v7, 0
	v_mov_b32_e32 v102, 0
	s_and_saveexec_b64 s[4:5], vcc
	s_cbranch_execz .LBB0_204
	v_mul_i32_i24_e32 v5, 16, v5
	v_sub_u32_e32 v3, v3, v5
	v_lshrrev_b32_e32 v5, 6, v0
	v_and_b32_e32 v5, 4, v5
	v_lshl_or_b32 v3, v3, 4, v5
	v_or3_b32 v12, v3, v1, v8
	v_ashrrev_i32_e32 v13, 31, v12
	v_lshlrev_b64 v[12:13], 8, v[12:13]
	v_ashrrev_i32_e32 v7, 31, v6
	v_lshl_add_u64 v[12:13], s[40:41], 0, v[12:13]
	v_lshl_add_u64 v[6:7], v[6:7], 2, v[12:13]
	global_load_dword v102, v[6:7], off
.LBB0_204:
	s_or_b64 exec, exec, s[4:5]
	v_ashrrev_i32_e32 v5, 31, v4
	v_add_u32_e32 v2, 0x300, v2
	v_lshl_add_u64 v[4:5], v[4:5], 1, s[0:1]
	v_ashrrev_i32_e32 v3, 9, v2
	v_mov_b32_e32 v108, v4
	v_mov_b32_e32 v109, v5
	v_lshrrev_b32_e32 v4, 28, v3
	v_add_u32_e32 v4, v3, v4
	v_ashrrev_i32_e32 v5, 4, v4
	v_lshl_or_b32 v4, v5, 5, v9
	v_cmp_gt_i32_e32 vcc, 64, v4
	v_mov_b32_e32 v103, 0
	s_and_saveexec_b64 s[4:5], vcc
	s_cbranch_execz .LBB0_206
	v_mul_i32_i24_e32 v5, 16, v5
	v_sub_u32_e32 v3, v3, v5
	v_lshrrev_b32_e32 v5, 6, v2
	v_and_b32_e32 v5, 4, v5
	v_lshl_or_b32 v3, v3, 4, v5
	v_or3_b32 v6, v3, v1, v8
	v_ashrrev_i32_e32 v7, 31, v6
	v_lshlrev_b64 v[6:7], 8, v[6:7]
	v_ashrrev_i32_e32 v5, 31, v4
	v_lshl_add_u64 v[6:7], s[40:41], 0, v[6:7]
	v_lshl_add_u64 v[4:5], v[4:5], 2, v[6:7]
	global_load_dword v103, v[4:5], off

.LBB0_208:
	s_andn2_b64 vcc, exec, s[4:5]
	s_cbranch_vccnz .LBB0_219
	s_lshl_b32 s0, s2, 10
	s_cmpk_gt_i32 s0, 0x3fff
	s_cbranch_scc1 .LBB0_219
	v_or_b32_e32 v2, s0, v0
	s_waitcnt lgkmcnt(0)
	v_ashrrev_i32_e32 v3, 9, v2
	v_lshrrev_b32_e32 v4, 30, v3
	v_add_u32_e32 v4, v3, v4
	v_bfe_u32 v9, v0, 3, 5
	v_ashrrev_i32_e32 v6, 2, v4
	v_lshlrev_b32_e32 v1, 1, v0
	v_lshl_or_b32 v4, v6, 5, v9
	s_movk_i32 s4, 0x100
	v_and_b32_e32 v1, 8, v1
	v_and_b32_e32 v8, 3, v0
	v_cmp_gt_i32_e32 vcc, s4, v4
	v_mov_b32_e32 v7, 0
	v_mov_b32_e32 v5, 0
	v_mov_b32_e32 v100, 0
	s_and_saveexec_b64 s[0:1], vcc
	s_cbranch_execz .LBB0_212
	v_mul_i32_i24_e32 v5, 4, v6
	v_sub_u32_e32 v3, v3, v5
	v_lshrrev_b32_e32 v5, 6, v0
	v_and_b32_e32 v5, 4, v5
	v_lshl_or_b32 v3, v3, 4, v5
	v_or3_b32 v10, v3, v1, v8
	v_ashrrev_i32_e32 v11, 31, v10
	v_lshlrev_b64 v[10:11], 10, v[10:11]
	v_ashrrev_i32_e32 v5, 31, v4
	v_lshl_add_u64 v[10:11], s[38:39], 0, v[10:11]
	v_lshl_add_u64 v[4:5], v[4:5], 2, v[10:11]
	global_load_dword v100, v[4:5], off
.LBB0_212:
	s_or_b64 exec, exec, s[0:1]
	s_add_u32 s0, s22, 0x8000
	s_addc_u32 s1, s23, 0
	v_ashrrev_i32_e32 v3, 31, v2
	v_add_u32_e32 v4, 0x100, v2
	v_lshl_add_u64 v[10:11], v[2:3], 1, s[0:1]
	v_ashrrev_i32_e32 v3, 9, v4
	v_mov_b32_e32 v104, v10
	v_mov_b32_e32 v105, v11
	v_lshrrev_b32_e32 v5, 30, v3
	v_add_u32_e32 v5, v3, v5
	v_ashrrev_i32_e32 v5, 2, v5
	v_lshl_or_b32 v6, v5, 5, v9
	v_cmp_gt_i32_e32 vcc, s4, v6
	v_mov_b32_e32 v101, 0
	s_and_saveexec_b64 s[4:5], vcc
	s_cbranch_execz .LBB0_214
	v_mul_i32_i24_e32 v5, 4, v5
	v_sub_u32_e32 v3, v3, v5
	v_lshrrev_b32_e32 v5, 6, v4
	v_and_b32_e32 v5, 4, v5
	v_lshl_or_b32 v3, v3, 4, v5
	v_or3_b32 v10, v3, v1, v8
	v_ashrrev_i32_e32 v11, 31, v10
	v_lshlrev_b64 v[10:11], 10, v[10:11]
	v_ashrrev_i32_e32 v7, 31, v6
	v_lshl_add_u64 v[10:11], s[38:39], 0, v[10:11]
	v_lshl_add_u64 v[6:7], v[6:7], 2, v[10:11]
	global_load_dword v101, v[6:7], off
.LBB0_214:
	s_or_b64 exec, exec, s[4:5]
	v_ashrrev_i32_e32 v5, 31, v4
	v_lshl_add_u64 v[4:5], v[4:5], 1, s[0:1]
	v_mov_b32_e32 v106, v4
	v_mov_b32_e32 v107, v5
	v_add_u32_e32 v4, 0x200, v2
	v_ashrrev_i32_e32 v3, 9, v4
	v_lshrrev_b32_e32 v5, 30, v3
	v_add_u32_e32 v5, v3, v5
	v_ashrrev_i32_e32 v5, 2, v5
	v_lshl_or_b32 v6, v5, 5, v9
	s_movk_i32 s6, 0x100
	v_cmp_gt_i32_e32 vcc, s6, v6
	v_mov_b32_e32 v10, 0
	v_mov_b32_e32 v7, 0
	v_mov_b32_e32 v102, 0
	s_and_saveexec_b64 s[4:5], vcc
	s_cbranch_execz .LBB0_216
	v_mul_i32_i24_e32 v5, 4, v5
	v_sub_u32_e32 v3, v3, v5
	v_lshrrev_b32_e32 v5, 6, v0
	v_and_b32_e32 v5, 4, v5
	v_lshl_or_b32 v3, v3, 4, v5
	v_or3_b32 v12, v3, v1, v8
	v_ashrrev_i32_e32 v13, 31, v12
	v_lshlrev_b64 v[12:13], 10, v[12:13]
	v_ashrrev_i32_e32 v7, 31, v6
	v_lshl_add_u64 v[12:13], s[38:39], 0, v[12:13]
	v_lshl_add_u64 v[6:7], v[6:7], 2, v[12:13]
	global_load_dword v102, v[6:7], off
.LBB0_216:
	s_or_b64 exec, exec, s[4:5]
	v_ashrrev_i32_e32 v5, 31, v4
	v_add_u32_e32 v2, 0x300, v2
	v_lshl_add_u64 v[4:5], v[4:5], 1, s[0:1]
	v_ashrrev_i32_e32 v3, 9, v2
	v_mov_b32_e32 v108, v4
	v_mov_b32_e32 v109, v5
	v_lshrrev_b32_e32 v4, 30, v3
	v_add_u32_e32 v4, v3, v4
	v_ashrrev_i32_e32 v5, 2, v4
	v_lshl_or_b32 v4, v5, 5, v9
	v_cmp_gt_i32_e32 vcc, s6, v4
	v_mov_b32_e32 v103, 0
	s_and_saveexec_b64 s[4:5], vcc
	s_cbranch_execz .LBB0_218
	v_mul_i32_i24_e32 v5, 4, v5
	v_sub_u32_e32 v3, v3, v5
	v_lshrrev_b32_e32 v5, 6, v2
	v_and_b32_e32 v5, 4, v5
	v_lshl_or_b32 v3, v3, 4, v5
	v_or3_b32 v6, v3, v1, v8
	v_ashrrev_i32_e32 v7, 31, v6
	v_lshlrev_b64 v[6:7], 10, v[6:7]
	v_ashrrev_i32_e32 v5, 31, v4
	v_lshl_add_u64 v[6:7], s[38:39], 0, v[6:7]
	v_lshl_add_u64 v[4:5], v[4:5], 2, v[6:7]
	global_load_dword v103, v[4:5], off

.LBB0_220:
	s_and_b64 vcc, exec, s[4:5]
	s_cbranch_vccz .LBB0_231
	s_lshl_b32 s2, s2, 10
	s_cmpk_gt_i32 s2, 0xfff
	s_cbranch_scc1 .LBB0_231
	s_lshl_b32 s4, s3, 12
	s_ashr_i32 s5, s4, 31
	s_lshl_b64 s[0:1], s[4:5], 2
	s_waitcnt lgkmcnt(0)
	s_add_u32 s0, s36, s0
	s_addc_u32 s1, s37, s1
	s_cmp_eq_u32 s3, 0
	v_mov_b32_e32 v1, 0x3eb8aa3b
	s_cselect_b64 vcc, -1, 0
	v_cndmask_b32_e32 v6, 1.0, v1, vcc
	v_or_b32_e32 v2, s2, v0
	v_lshlrev_b32_e32 v1, 1, v0
	v_and_b32_e32 v7, 8, v1
	v_ashrrev_i32_e32 v1, 9, v2
	v_lshrrev_b32_e32 v3, 30, v1
	v_add_u32_e32 v3, v1, v3
	v_bfe_u32 v9, v0, 3, 5
	v_ashrrev_i32_e32 v3, 2, v3
	v_lshl_or_b32 v4, v3, 5, v9
	v_and_b32_e32 v8, 3, v0
	v_cmp_gt_i32_e32 vcc, 64, v4
	v_mov_b32_e32 v11, 0
	v_lshrrev_b32_e32 v10, 6, v0
	v_mov_b32_e32 v5, 0
	v_mov_b32_e32 v100, 0
	s_and_saveexec_b64 s[2:3], vcc
	s_cbranch_execz .LBB0_224
	v_mul_i32_i24_e32 v0, 4, v3
	v_sub_u32_e32 v0, v1, v0
	v_and_b32_e32 v1, 4, v10
	v_lshl_or_b32 v0, v0, 4, v1
	v_or3_b32 v0, v0, v7, v8
	v_ashrrev_i32_e32 v1, 31, v0
	v_lshlrev_b64 v[0:1], 8, v[0:1]
	v_ashrrev_i32_e32 v5, 31, v4
	v_lshl_add_u64 v[0:1], s[0:1], 0, v[0:1]
	v_lshl_add_u64 v[0:1], v[4:5], 2, v[0:1]
	global_load_dword v100, v[0:1], off
.LBB0_224:
	s_or_b64 exec, exec, s[2:3]
	s_lshl_b64 s[2:3], s[4:5], 1
	s_add_u32 s2, s22, s2
	s_addc_u32 s3, s23, s3
	v_ashrrev_i32_e32 v3, 31, v2
	v_lshl_add_u64 v[0:1], v[2:3], 1, s[2:3]
	v_add_u32_e32 v3, 0x100, v2
	v_mov_b32_e32 v112, v6
	v_mov_b32_e32 v104, v0
	v_mov_b32_e32 v105, v1
	v_ashrrev_i32_e32 v5, 9, v3
	v_lshrrev_b32_e32 v4, 30, v5
	v_add_u32_e32 v4, v5, v4
	v_ashrrev_i32_e32 v12, 2, v4
	v_lshl_or_b32 v4, v12, 5, v9
	v_cmp_gt_i32_e32 vcc, 64, v4
	v_mov_b32_e32 v101, 0
	s_and_saveexec_b64 s[2:3], vcc
	s_cbranch_execz .LBB0_226
	v_mul_i32_i24_e32 v11, 4, v12
	v_lshrrev_b32_e32 v3, 6, v3
	v_sub_u32_e32 v5, v5, v11
	v_and_b32_e32 v3, 4, v3
	v_lshl_or_b32 v3, v5, 4, v3
	v_or3_b32 v12, v3, v7, v8
	v_ashrrev_i32_e32 v13, 31, v12
	v_lshlrev_b64 v[12:13], 8, v[12:13]
	v_ashrrev_i32_e32 v5, 31, v4
	v_lshl_add_u64 v[12:13], s[0:1], 0, v[12:13]
	v_lshl_add_u64 v[4:5], v[4:5], 2, v[12:13]
	global_load_dword v101, v[4:5], off
.LBB0_226:
	s_or_b64 exec, exec, s[2:3]
	v_add_u32_e32 v3, 0x200, v2
	v_ashrrev_i32_e32 v5, 9, v3
	v_lshrrev_b32_e32 v3, 30, v5
	v_add_u32_e32 v3, v5, v3
	v_mov_b32_e32 v106, v0
	v_mov_b32_e32 v107, v1
	v_ashrrev_i32_e32 v11, 2, v3
	v_lshl_or_b32 v4, v11, 5, v9
	v_cmp_gt_i32_e32 vcc, 64, v4
	v_mov_b32_e32 v3, 0
	v_mov_b32_e32 v12, 0
	v_mov_b32_e32 v102, 0
	s_and_saveexec_b64 s[2:3], vcc
	s_cbranch_execz .LBB0_228
	v_mul_i32_i24_e32 v11, 4, v11
	v_sub_u32_e32 v5, v5, v11
	v_and_b32_e32 v10, 4, v10
	v_lshl_or_b32 v5, v5, 4, v10
	v_or3_b32 v10, v5, v7, v8
	v_ashrrev_i32_e32 v11, 31, v10
	v_lshlrev_b64 v[10:11], 8, v[10:11]
	v_ashrrev_i32_e32 v5, 31, v4
	v_lshl_add_u64 v[10:11], s[0:1], 0, v[10:11]
	v_lshl_add_u64 v[4:5], v[4:5], 2, v[10:11]
	global_load_dword v102, v[4:5], off
.LBB0_228:
	s_or_b64 exec, exec, s[2:3]
	v_add_u32_e32 v4, 0x300, v2
	v_ashrrev_i32_e32 v5, 9, v4
	v_lshrrev_b32_e32 v2, 30, v5
	v_add_u32_e32 v2, v5, v2
	v_ashrrev_i32_e32 v10, 2, v2
	v_lshl_or_b32 v2, v10, 5, v9
	v_cmp_gt_i32_e32 vcc, 64, v2
	v_mov_b32_e32 v108, v0
	v_mov_b32_e32 v109, v1
	v_mov_b32_e32 v103, 0
	s_and_saveexec_b64 s[2:3], vcc
	s_cbranch_execz .LBB0_230
	v_mul_i32_i24_e32 v3, 4, v10
	v_lshrrev_b32_e32 v4, 6, v4
	v_sub_u32_e32 v3, v5, v3
	v_and_b32_e32 v4, 4, v4
	v_lshl_or_b32 v3, v3, 4, v4
	v_or3_b32 v4, v3, v7, v8
	v_ashrrev_i32_e32 v5, 31, v4
	v_lshlrev_b64 v[4:5], 8, v[4:5]
	v_ashrrev_i32_e32 v3, 31, v2
	v_lshl_add_u64 v[4:5], s[0:1], 0, v[4:5]
	v_lshl_add_u64 v[2:3], v[2:3], 2, v[4:5]
	global_load_dword v103, v[2:3], off
.LBB0_230:
	s_or_b64 exec, exec, s[2:3]
	s_waitcnt vmcnt(0)
	v_fma_mixlo_f16 v100, v112, v100, 0
	v_fma_mixlo_f16 v101, v112, v101, 0
	v_fma_mixlo_f16 v102, v112, v102, 0
	v_fma_mixlo_f16 v103, v112, v103, 0
	global_store_short v[104:105], v100, off
	global_store_short v[106:107], v101, off offset:512
	global_store_short v[108:109], v102, off offset:1024
	global_store_short v[0:1], v103, off offset:1536

_Z10k2_featurePKfPKDF16_S0_S0_S0_S0_S0_S0_PKyS0_S0_S0_S0_S0_S0_S0_PfS5_S5_S5_S5_:
	s_cmp_lg_u32 s2, 0
	s_cbranch_scc1 .Lmy_z0
	s_load_dwordx2 s[4:5], s[0:1], 0xa0
	v_mov_b32_e32 v1, 0
	v_lshlrev_b32_e32 v2, 2, v0
	s_movk_i32 s6, 0xa0
	v_cmp_gt_u32_e32 vcc, s6, v0
	s_waitcnt lgkmcnt(0)
	s_and_saveexec_b64 s[6:7], vcc
	global_store_dword v2, v1, s[4:5] offset:1536
	s_or_b64 exec, exec, s[6:7]
.Lmy_z0:
	v_readfirstlane_b32 s14, v0
	s_load_dwordx2 s[4:5], s[0:1], 0x0
	s_load_dwordx4 s[8:11], s[0:1], 0x18
	s_load_dwordx2 s[6:7], s[0:1], 0x40
	s_lshr_b32 s28, s14, 8
	s_lshl_b32 s20, s2, 1
	s_add_i32 s12, s28, s20
	s_lshr_b32 s2, s14, 1
	v_and_b32_e32 v174, 31, v0
	v_bfe_u32 v164, v0, 5, 1
	s_and_b32 s15, s2, 0x60
	s_ashr_i32 s13, s12, 31
	v_or_b32_e32 v1, s15, v174
	v_lshlrev_b32_e32 v2, 3, v164
	s_lshl_b64 s[2:3], s[12:13], 13
	v_lshl_or_b32 v3, v1, 4, v2
	v_lshl_or_b32 v118, v1, 6, s2
	v_mov_b32_e32 v119, s3
	s_waitcnt lgkmcnt(0)
	global_load_dwordx2 v[66:67], v3, s[6:7]
	v_lshl_add_u64 v[4:5], v[118:119], 1, s[4:5]
	v_mov_b32_e32 v3, 0
	v_lshl_add_u64 v[2:3], v[4:5], 0, v[2:3]
	global_load_dwordx2 v[110:111], v[2:3], off
	global_load_dwordx2 v[112:113], v[2:3], off offset:16
	global_load_dwordx2 v[106:107], v[2:3], off offset:32
	global_load_dwordx2 v[108:109], v[2:3], off offset:48
	global_load_dwordx2 v[102:103], v[2:3], off offset:64
	global_load_dwordx2 v[104:105], v[2:3], off offset:80
	global_load_dwordx2 v[98:99], v[2:3], off offset:96
	global_load_dwordx2 v[100:101], v[2:3], off offset:112
	s_load_dwordx2 s[4:5], s[0:1], 0x30
	s_movk_i32 s2, 0xff
	v_cmp_lt_u32_e32 vcc, s2, v0
	s_and_saveexec_b64 s[2:3], vcc
	s_xor_b64 s[6:7], exec, s[2:3]
	s_cbranch_execz .LBB2_14
	s_movk_i32 s2, 0x1ff
	v_cmp_lt_u32_e64 s[2:3], s2, v0
	s_and_saveexec_b64 s[16:17], s[2:3]
	s_xor_b64 s[16:17], exec, s[16:17]
	s_cbranch_execz .LBB2_11
	s_movk_i32 s2, 0x2ff
	v_cmp_lt_u32_e64 s[2:3], s2, v0
	s_and_saveexec_b64 s[18:19], s[2:3]
	s_xor_b64 s[18:19], exec, s[18:19]
	s_cbranch_execz .LBB2_8
	s_movk_i32 s2, 0x33f
	v_cmp_lt_u32_e64 s[2:3], s2, v0
	v_mov_b32_e32 v3, 0
	s_and_saveexec_b64 s[22:23], s[2:3]
	s_xor_b64 s[2:3], exec, s[22:23]
	s_cbranch_execz .LBB2_5
	v_lshlrev_b32_e32 v2, 2, v0
	s_movk_i32 s22, 0xf300
	s_waitcnt lgkmcnt(0)
	v_lshl_add_u64 v[2:3], s[4:5], 0, v[2:3]
	s_mov_b32 s23, -1
	v_lshl_add_u64 v[4:5], v[2:3], 0, s[22:23]

_Z5k3_vqPKDF16_S0_S0_S0_PKfPiPfS3_S4_:
	s_and_b32 s52, s2, 7
	s_lshl_b32 s52, s52, 6
	v_readfirstlane_b32 s3, v0
	s_lshr_b32 s12, s3, 6
	s_lshl_b32 s3, s2, 5
	v_bfe_u32 v36, v0, 5, 1
	s_and_b32 s3, s3, 0xe0
	s_lshr_b32 s8, s2, 3
	s_load_dwordx4 s[4:7], s[0:1], 0x0
	s_add_i32 s3, s3, s8
	v_lshlrev_b32_e32 v2, 3, v36
	v_mov_b32_e32 v35, 0
	v_and_b32_e32 v1, 31, v0
	s_lshl_b32 s3, s3, 5
	v_lshl_or_b32 v18, s12, 5, v2
	v_mov_b32_e32 v19, v35
	v_or_b32_e32 v34, s3, v1
	v_lshlrev_b64 v[2:3], 13, v[18:19]
	v_lshl_add_u64 v[2:3], v[2:3], 0, v[34:35]
	v_lshlrev_b64 v[4:5], 1, v[2:3]
	s_waitcnt lgkmcnt(0)
	v_lshl_add_u64 v[2:3], s[4:5], 0, v[4:5]
	v_lshl_add_u64 v[4:5], s[6:7], 0, v[4:5]
	global_load_ushort v2, v[2:3], off
	v_cmp_gt_u32_e32 vcc, 16, v0
	global_load_ushort v3, v[4:5], off
	v_or_b32_e32 v4, 1, v18
	v_mov_b32_e32 v5, v35
	v_lshlrev_b64 v[4:5], 13, v[4:5]
	v_lshl_add_u64 v[4:5], v[4:5], 0, v[34:35]
	v_lshlrev_b64 v[6:7], 1, v[4:5]
	v_lshl_add_u64 v[4:5], s[4:5], 0, v[6:7]
	v_lshl_add_u64 v[6:7], s[6:7], 0, v[6:7]
	global_load_ushort v4, v[4:5], off
	v_lshlrev_b32_e32 v37, 2, v0
	global_load_ushort v5, v[6:7], off
	v_or_b32_e32 v6, 2, v18
	v_mov_b32_e32 v7, v35
	v_lshlrev_b64 v[6:7], 13, v[6:7]
	v_lshl_add_u64 v[6:7], v[6:7], 0, v[34:35]
	v_lshlrev_b64 v[8:9], 1, v[6:7]
	v_lshl_add_u64 v[6:7], s[4:5], 0, v[8:9]
	v_lshl_add_u64 v[8:9], s[6:7], 0, v[8:9]
	global_load_ushort v6, v[6:7], off
	s_nop 0
	global_load_ushort v7, v[8:9], off
	v_or_b32_e32 v8, 3, v18
	v_mov_b32_e32 v9, v35
	v_lshlrev_b64 v[8:9], 13, v[8:9]
	v_lshl_add_u64 v[8:9], v[8:9], 0, v[34:35]
	v_lshlrev_b64 v[10:11], 1, v[8:9]
	v_lshl_add_u64 v[8:9], s[4:5], 0, v[10:11]
	v_lshl_add_u64 v[10:11], s[6:7], 0, v[10:11]
	global_load_ushort v8, v[8:9], off
	s_nop 0
	global_load_ushort v9, v[10:11], off
	v_or_b32_e32 v10, 4, v18
	v_mov_b32_e32 v11, v35
	v_lshlrev_b64 v[10:11], 13, v[10:11]
	v_lshl_add_u64 v[10:11], v[10:11], 0, v[34:35]
	v_lshlrev_b64 v[12:13], 1, v[10:11]
	v_lshl_add_u64 v[10:11], s[4:5], 0, v[12:13]
	v_lshl_add_u64 v[12:13], s[6:7], 0, v[12:13]
	global_load_ushort v10, v[10:11], off
	s_nop 0
	global_load_ushort v11, v[12:13], off
	v_or_b32_e32 v12, 5, v18
	v_mov_b32_e32 v13, v35
	v_lshlrev_b64 v[12:13], 13, v[12:13]
	v_lshl_add_u64 v[12:13], v[12:13], 0, v[34:35]
	v_lshlrev_b64 v[14:15], 1, v[12:13]
	v_lshl_add_u64 v[12:13], s[4:5], 0, v[14:15]
	v_lshl_add_u64 v[14:15], s[6:7], 0, v[14:15]
	global_load_ushort v12, v[12:13], off
	s_nop 0
	global_load_ushort v13, v[14:15], off
	v_or_b32_e32 v14, 6, v18
	v_mov_b32_e32 v15, v35
	v_lshlrev_b64 v[14:15], 13, v[14:15]
	v_lshl_add_u64 v[14:15], v[14:15], 0, v[34:35]
	v_lshlrev_b64 v[16:17], 1, v[14:15]
	v_lshl_add_u64 v[14:15], s[4:5], 0, v[16:17]
	v_lshl_add_u64 v[16:17], s[6:7], 0, v[16:17]
	global_load_ushort v14, v[14:15], off
	s_nop 0
	global_load_ushort v15, v[16:17], off
	v_or_b32_e32 v16, 7, v18
	v_mov_b32_e32 v17, v35
	v_lshlrev_b64 v[16:17], 13, v[16:17]
	v_lshl_add_u64 v[16:17], v[16:17], 0, v[34:35]
	v_lshlrev_b64 v[20:21], 1, v[16:17]
	v_lshl_add_u64 v[16:17], s[4:5], 0, v[20:21]
	v_lshl_add_u64 v[20:21], s[6:7], 0, v[20:21]
	global_load_ushort v16, v[16:17], off
	s_nop 0
	global_load_ushort v17, v[20:21], off
	v_or_b32_e32 v20, 16, v18
	v_mov_b32_e32 v21, v35
	v_lshlrev_b64 v[20:21], 13, v[20:21]
	v_lshl_add_u64 v[20:21], v[20:21], 0, v[34:35]
	v_lshlrev_b64 v[20:21], 1, v[20:21]
	v_lshl_add_u64 v[22:23], s[4:5], 0, v[20:21]
	v_lshl_add_u64 v[20:21], s[6:7], 0, v[20:21]
	global_load_ushort v39, v[20:21], off
	v_or_b32_e32 v20, 17, v18
	v_mov_b32_e32 v21, v35
	v_lshlrev_b64 v[20:21], 13, v[20:21]
	v_lshl_add_u64 v[20:21], v[20:21], 0, v[34:35]
	v_lshlrev_b64 v[20:21], 1, v[20:21]
	global_load_ushort v38, v[22:23], off
	v_lshl_add_u64 v[22:23], s[4:5], 0, v[20:21]
	v_lshl_add_u64 v[20:21], s[6:7], 0, v[20:21]
	global_load_ushort v41, v[20:21], off
	v_or_b32_e32 v20, 18, v18
	v_mov_b32_e32 v21, v35
	v_lshlrev_b64 v[20:21], 13, v[20:21]
	v_lshl_add_u64 v[20:21], v[20:21], 0, v[34:35]
	v_lshlrev_b64 v[20:21], 1, v[20:21]
	global_load_ushort v40, v[22:23], off
	v_lshl_add_u64 v[22:23], s[4:5], 0, v[20:21]
	v_lshl_add_u64 v[20:21], s[6:7], 0, v[20:21]
	global_load_ushort v43, v[20:21], off
	v_or_b32_e32 v20, 19, v18
	v_mov_b32_e32 v21, v35
	v_lshlrev_b64 v[20:21], 13, v[20:21]
	v_lshl_add_u64 v[20:21], v[20:21], 0, v[34:35]
	v_lshlrev_b64 v[20:21], 1, v[20:21]
	global_load_ushort v42, v[22:23], off
	v_lshl_add_u64 v[22:23], s[4:5], 0, v[20:21]
	v_lshl_add_u64 v[20:21], s[6:7], 0, v[20:21]
	global_load_ushort v45, v[20:21], off
	v_or_b32_e32 v20, 20, v18
	v_mov_b32_e32 v21, v35
	v_lshlrev_b64 v[20:21], 13, v[20:21]
	v_lshl_add_u64 v[20:21], v[20:21], 0, v[34:35]
	v_lshlrev_b64 v[20:21], 1, v[20:21]
	global_load_ushort v44, v[22:23], off
	v_lshl_add_u64 v[22:23], s[4:5], 0, v[20:21]
	v_lshl_add_u64 v[20:21], s[6:7], 0, v[20:21]
	global_load_ushort v47, v[20:21], off
	v_or_b32_e32 v20, 21, v18
	v_mov_b32_e32 v21, v35
	v_lshlrev_b64 v[20:21], 13, v[20:21]
	v_lshl_add_u64 v[20:21], v[20:21], 0, v[34:35]
	v_lshlrev_b64 v[20:21], 1, v[20:21]
	global_load_ushort v46, v[22:23], off
	v_lshl_add_u64 v[22:23], s[4:5], 0, v[20:21]
	v_lshl_add_u64 v[20:21], s[6:7], 0, v[20:21]
	global_load_ushort v49, v[20:21], off
	v_or_b32_e32 v20, 22, v18
	v_mov_b32_e32 v21, v35
	v_lshlrev_b64 v[20:21], 13, v[20:21]
	v_or_b32_e32 v18, 23, v18
	v_lshl_add_u64 v[20:21], v[20:21], 0, v[34:35]
	v_lshlrev_b64 v[18:19], 13, v[18:19]
	v_lshlrev_b64 v[20:21], 1, v[20:21]
	v_lshl_add_u64 v[18:19], v[18:19], 0, v[34:35]
	global_load_ushort v48, v[22:23], off
	v_lshl_add_u64 v[22:23], s[4:5], 0, v[20:21]
	v_lshl_add_u64 v[20:21], s[6:7], 0, v[20:21]
	v_lshlrev_b64 v[18:19], 1, v[18:19]
	global_load_ushort v51, v[20:21], off
	v_lshl_add_u64 v[20:21], s[4:5], 0, v[18:19]
	v_lshl_add_u64 v[18:19], s[6:7], 0, v[18:19]
	global_load_ushort v50, v[22:23], off
	global_load_ushort v52, v[20:21], off
	global_load_ushort v53, v[18:19], off
	s_and_saveexec_b64 s[4:5], vcc
	v_lshlrev_b32_e32 v18, 2, v0
	ds_write_b32 v18, v35 offset:56704
	s_or_b64 exec, exec, s[4:5]
	s_load_dwordx4 s[8:11], s[0:1], 0x10
	v_and_b32_e32 v18, 0x3e0, v0
	v_and_b32_e32 v35, 63, v0
	v_cmp_eq_u32_e64 s[4:5], 64, v18
	s_and_saveexec_b64 s[6:7], s[4:5]
	s_cbranch_execz .LBB3_4
	s_load_dwordx2 s[4:5], s[0:1], 0x20
	v_subrev_u32_e32 v18, 64, v0
	v_mov_b32_e32 v19, 0
	s_waitcnt lgkmcnt(0)
	v_lshl_add_u64 v[20:21], v[18:19], 2, s[4:5]
	global_load_dword v75, v[20:21], off
	v_lshlrev_b32_e32 v74, 2, v18

.LBB3_6:
	s_or_b64 exec, exec, s[4:5]
	v_lshlrev_b32_e32 v10, 9, v36
	v_lshlrev_b32_e32 v1, 2, v1
	v_add3_u32 v1, s12, v10, v1
	ds_write2_b32 v1, v2, v3 offset0:64 offset1:96
	v_add_u32_e32 v2, 0x800, v1
	ds_write2_b32 v2, v26, v27 offset0:64 offset1:96
	ds_write2_b32 v1, v4, v5 offset0:128 offset1:160
	ds_write2_b32 v2, v28, v29 offset0:128 offset1:160
	v_add_u32_e32 v2, 0x400, v1
	v_add_u32_e32 v1, 0xc00, v1
	ds_write2_b32 v2, v6, v7 offset0:64 offset1:96
	ds_write2_b32 v1, v30, v31 offset0:64 offset1:96
	ds_write2_b32 v2, v8, v9 offset0:128 offset1:160
	ds_write2_b32 v1, v32, v33 offset0:128 offset1:160
	v_add_u32_e32 v1, 0xfffffd00, v0
	s_mov_b64 s[4:5], 0
	s_movk_i32 s6, 0x13f
	v_and_b32_e32 v73, 0x3e0, v0
	v_cmp_eq_u32_e64 s[48:49], 64, v73
	s_and_saveexec_b64 s[50:51], s[48:49]
	s_waitcnt vmcnt(0)
	ds_write_b32 v74, v75 offset:56576
	s_or_b64 exec, exec, s[50:51]
	s_waitcnt lgkmcnt(0)
	s_barrier

.LBB3_11:
	s_or_b64 exec, exec, s[38:39]
	s_waitcnt lgkmcnt(0)
	s_barrier
	s_and_saveexec_b64 s[0:1], vcc
	s_cbranch_execz .LBB3_14
	v_lshlrev_b32_e32 v0, 2, v0
	ds_read_b32 v1, v0 offset:56704
	s_waitcnt lgkmcnt(0)
	v_cmp_ne_u32_e32 vcc, 0, v1
	s_and_b64 exec, exec, vcc
	s_cbranch_execz .LBB3_14
	s_add_u32 s44, s42, s52
	s_addc_u32 s45, s43, 0
	s_add_u32 s44, s44, 0xfffffc80
	s_addc_u32 s45, s45, -1
	global_atomic_add v0, v1, s[44:45]

	.amdhsa_kernel _Z5k3_vqPKDF16_S0_S0_S0_PKfPiPfS3_S4_
		.amdhsa_group_segment_fixed_size 56768
		.amdhsa_private_segment_fixed_size 0
		.amdhsa_kernarg_size 72
		.amdhsa_user_sgpr_count 2
		.amdhsa_user_sgpr_dispatch_ptr 0
		.amdhsa_user_sgpr_queue_ptr 0
		.amdhsa_user_sgpr_kernarg_segment_ptr 1
		.amdhsa_user_sgpr_dispatch_id 0
		.amdhsa_user_sgpr_kernarg_preload_length 0
		.amdhsa_user_sgpr_kernarg_preload_offset 0
		.amdhsa_user_sgpr_private_segment_size 0
		.amdhsa_uses_dynamic_stack 0
		.amdhsa_enable_private_segment 0
		.amdhsa_system_sgpr_workgroup_id_x 1
		.amdhsa_system_sgpr_workgroup_id_y 0
		.amdhsa_system_sgpr_workgroup_id_z 0
		.amdhsa_system_sgpr_workgroup_info 0
		.amdhsa_system_vgpr_workitem_id 0
		.amdhsa_next_free_vgpr 76
		.amdhsa_next_free_sgpr 91
		.amdhsa_accum_offset 76
		.amdhsa_reserve_vcc 1
		.amdhsa_float_round_mode_32 0
		.amdhsa_float_round_mode_16_64 0
		.amdhsa_float_denorm_mode_32 3
		.amdhsa_float_denorm_mode_16_64 3
		.amdhsa_dx10_clamp 1
		.amdhsa_ieee_mode 1
		.amdhsa_fp16_overflow 0
		.amdhsa_tg_split 0
		.amdhsa_exception_fp_ieee_invalid_op 0
		.amdhsa_exception_fp_denorm_src 0
		.amdhsa_exception_fp_ieee_div_zero 0
		.amdhsa_exception_fp_ieee_overflow 0
		.amdhsa_exception_fp_ieee_underflow 0
		.amdhsa_exception_fp_ieee_inexact 0
		.amdhsa_exception_int_div_zero 0
	.end_amdhsa_kernel

_Z7k5_convPKDF16_PKiS0_PKfS4_S4_S4_S4_S4_S4_S4_PfS4_S4_S2_S2_S4_PiS5_S5_:
	s_and_b32 s45, s2, 7
	s_lshl_b32 s45, s45, 3
	s_load_dwordx2 s[46:47], s[0:1], 0x58
	v_lshrrev_b32_e32 v2, 6, v0
	s_lshl_b32 s3, s2, 5
	v_readfirstlane_b32 s34, v2
	s_and_b32 s3, s3, 0xe0
	s_lshr_b32 s8, s2, 3
	s_add_i32 s3, s3, s8
	s_ashr_i32 s33, s34, 1
	s_lshr_b32 s8, s3, 6
	s_lshl_b32 s3, s3, 1
	s_mul_hi_i32 s43, s33, 0x55555556
	s_and_b32 s44, s3, 0x7e
	s_lshr_b32 s3, s43, 31
	s_add_i32 s43, s43, s3
	s_mul_i32 s3, s43, 3
	v_and_b32_e32 v1, 31, v0
	s_sub_i32 s3, s33, s3
	s_load_dwordx2 s[4:5], s[0:1], 0x0
	s_load_dwordx8 s[24:31], s[0:1], 0x30
	s_load_dwordx2 s[6:7], s[0:1], 0x50
	v_lshl_or_b32 v47, s3, 5, v1
	s_mulk_i32 s8, 0x60
	s_add_i32 s9, s43, s44
	v_add_u32_e32 v3, s8, v47
	v_lshl_add_u32 v4, v3, 7, s9
	v_ashrrev_i32_e32 v5, 31, v4
	v_lshlrev_b64 v[4:5], 2, v[4:5]
	s_movk_i32 s3, 0x60
	s_waitcnt lgkmcnt(0)
	v_lshl_add_u64 v[6:7], s[30:31], 0, v[4:5]
	v_lshl_add_u64 v[4:5], s[6:7], 0, v[4:5]
	v_mul_u32_u24_e32 v3, 0x2ab, v0
	global_load_dword v46, v[4:5], off
	v_mul_lo_u16_sdwa v4, v3, s3 dst_sel:DWORD dst_unused:UNUSED_PAD src0_sel:WORD_1 src1_sel:DWORD
	v_sub_u16_e32 v4, v0, v4
	s_movk_i32 s6, 0x180
	v_mul_lo_u16_sdwa v3, v3, s6 dst_sel:DWORD dst_unused:UNUSED_PAD src0_sel:WORD_1 src1_sel:DWORD
	v_add_u32_e32 v4, s8, v4
	v_add_lshl_u32 v3, v4, v3, 1
	v_add_u32_e32 v4, 0x300, v0
	v_mul_u32_u24_e32 v5, 0x2ab, v4
	global_load_dword v45, v[6:7], off
	v_mul_lo_u16_sdwa v6, v5, s3 dst_sel:DWORD dst_unused:UNUSED_PAD src0_sel:WORD_1 src1_sel:DWORD
	v_sub_u16_e32 v4, v4, v6
	v_mul_lo_u16_sdwa v5, v5, s6 dst_sel:DWORD dst_unused:UNUSED_PAD src0_sel:WORD_1 src1_sel:DWORD
	v_add_u32_e32 v4, s8, v4
	v_add_lshl_u32 v4, v4, v5, 1
	global_load_ushort v9, v3, s[4:5]
	global_load_ushort v10, v4, s[4:5]
	s_load_dwordx2 s[30:31], s[0:1], 0x98
	s_load_dwordx2 s[6:7], s[0:1], 0x80
	s_load_dwordx8 s[16:23], s[0:1], 0x60
	s_load_dwordx8 s[8:15], s[0:1], 0x10
	s_load_dword s42, s[28:29], 0x0
	s_movk_i32 s3, 0x100
	v_and_b32_e32 v44, 63, v0
	v_cmp_gt_u32_e32 vcc, s3, v0
	v_mov_b32_e32 v11, 0
	s_and_saveexec_b64 s[28:29], vcc
	s_cbranch_execz .LBB4_4
	v_add3_u32 v3, s44, -1, v2
	s_movk_i32 s3, 0x80
	v_cmp_gt_u32_e64 s[4:5], s3, v3
	v_mov_b32_e32 v11, 0
	s_and_saveexec_b64 s[36:37], s[4:5]
	s_cbranch_execz .LBB4_3
	s_load_dwordx2 s[4:5], s[0:1], 0x8
	v_lshl_or_b32 v4, v44, 7, v3
	v_mov_b32_e32 v5, 0
	s_waitcnt lgkmcnt(0)
	v_lshl_add_u64 v[4:5], v[4:5], 2, s[4:5]
	global_load_dword v11, v[4:5], off

.LBB4_32:
	v_lshlrev_b32_e32 v6, 2, v44
	global_load_dword v5, v6, s[16:17]
	global_load_dword v7, v6, s[16:17] offset:256
	global_load_dword v3, v6, s[16:17] offset:512
	global_load_dword v14, v6, s[18:19] offset:768
	global_load_dword v16, v6, s[18:19] offset:512
	global_load_dword v18, v6, s[18:19] offset:256
	global_load_dword v2, v6, s[18:19]
	global_load_dword v19, v6, s[16:17] offset:768
	global_load_dword v17, v6, s[16:17] offset:1024
	global_load_dword v15, v6, s[16:17] offset:1280
	v_mov_b32_e32 v4, 0
	v_cmp_gt_u32_e64 s[2:3], 16, v44
	v_mov_b32_e32 v8, -1
	s_waitcnt vmcnt(9)
	v_add_f32_e32 v5, 0, v5
	s_waitcnt vmcnt(8)
	v_add_f32_e32 v5, v5, v7
	s_waitcnt vmcnt(3)
	v_pk_add_f32 v[2:3], v[4:5], v[2:3]
	s_waitcnt vmcnt(2)
	v_pk_add_f32 v[2:3], v[2:3], v[18:19]
	v_mov_b32_e32 v5, v4
	s_waitcnt vmcnt(1)
	v_pk_add_f32 v[2:3], v[2:3], v[16:17]
	s_waitcnt vmcnt(0)
	v_pk_add_f32 v[2:3], v[2:3], v[14:15]
	v_mov_b32_e32 v80, 0
	v_mov_b32_e32 v81, 0
	v_mov_b32_e32 v82, 0
	v_mov_b32_e32 v83, 0
	v_mov_b32_e32 v84, 0
	v_mov_b32_e32 v85, 0
	v_mov_b32_e32 v86, 0
	v_mov_b32_e32 v87, 0
	s_and_saveexec_b64 s[10:11], s[2:3]
	s_cbranch_execz .LBB4_34
	global_load_dword v80, v6, s[46:47] offset:128
	global_load_dword v81, v6, s[46:47] offset:192
	global_load_dword v82, v6, s[46:47] offset:256
	global_load_dword v83, v6, s[46:47] offset:320
	global_load_dword v84, v6, s[46:47] offset:384
	global_load_dword v85, v6, s[46:47] offset:448
	global_load_dword v86, v6, s[46:47] offset:512
	global_load_dword v87, v6, s[46:47] offset:576
	global_load_dword v8, v6, s[22:23]
	global_load_dword v4, v6, s[6:7]

.LBB4_43:
	s_or_b64 exec, exec, s[2:3]
	v_lshlrev_b32_e32 v42, 4, v44
	v_mov_b32_e32 v43, 0
	s_waitcnt vmcnt(6)
	s_waitcnt lgkmcnt(0)
	s_barrier
	s_load_dwordx4 s[8:11], s[0:1], 0x88
	s_andn2_b64 vcc, exec, s[4:5]
	v_mbcnt_lo_u32_b32 v43, -1, 0
	s_cbranch_vccnz .LBB4_47
	v_mbcnt_hi_u32_b32 v7, -1, v43
	v_and_b32_e32 v6, 64, v7
	v_add_u32_e32 v10, 64, v6
	v_xor_b32_e32 v6, 1, v7
	v_cmp_lt_i32_e32 vcc, v6, v10
	v_xor_b32_e32 v9, 2, v7
	v_xor_b32_e32 v16, 32, v7
	v_cndmask_b32_e32 v6, v7, v6, vcc
	v_lshlrev_b32_e32 v11, 2, v6
	ds_bpermute_b32 v6, v11, v3
	v_cmp_lt_i32_e32 vcc, v9, v10
	v_add_u32_e32 v5, v80, v81
	v_add3_u32 v5, v5, v82, v83
	v_add3_u32 v5, v5, v84, v85
	v_add3_u32 v5, v5, v86, v87
	v_cvt_f32_i32_e32 v19, v5
	s_mov_b32 s13, 0x800000
	s_mov_b32 s12, 0x3f317217
	s_waitcnt lgkmcnt(0)
	v_add_f32_e32 v3, v3, v6
	v_cndmask_b32_e32 v6, v7, v9, vcc
	v_lshlrev_b32_e32 v12, 2, v6
	ds_bpermute_b32 v6, v12, v3
	v_xor_b32_e32 v9, 4, v7
	v_cmp_lt_i32_e32 vcc, v9, v10
	s_mov_b32 s14, 0x7f800000
	s_waitcnt lgkmcnt(0)
	v_add_f32_e32 v3, v3, v6
	v_cndmask_b32_e32 v6, v7, v9, vcc
	v_lshlrev_b32_e32 v13, 2, v6
	ds_bpermute_b32 v6, v13, v3
	v_xor_b32_e32 v9, 8, v7
	v_cmp_lt_i32_e32 vcc, v9, v10
	s_waitcnt lgkmcnt(0)
	v_add_f32_e32 v3, v3, v6
	v_cndmask_b32_e32 v6, v7, v9, vcc
	v_lshlrev_b32_e32 v14, 2, v6
	ds_bpermute_b32 v6, v14, v3
	v_xor_b32_e32 v9, 16, v7
	v_cmp_lt_i32_e32 vcc, v9, v10
	s_waitcnt lgkmcnt(0)
	v_add_f32_e32 v3, v3, v6
	v_cndmask_b32_e32 v6, v7, v9, vcc
	v_lshlrev_b32_e32 v15, 2, v6
	ds_bpermute_b32 v9, v15, v3
	v_cmp_lt_i32_e32 vcc, v16, v10
	ds_bpermute_b32 v6, v11, v2
	s_waitcnt lgkmcnt(0)
	v_add_f32_e32 v9, v3, v9
	v_lshlrev_b32_e32 v3, 2, v7
	v_and_b32_e32 v3, 0x100, v3
	v_cndmask_b32_e32 v10, v7, v16, vcc
	ds_bpermute_b32 v7, v3, v8
	ds_bpermute_b32 v16, v3, v5
	ds_bpermute_b32 v17, v3, v8 offset:4
	ds_bpermute_b32 v18, v3, v5 offset:4
	ds_bpermute_b32 v20, v3, v8 offset:12
	s_waitcnt lgkmcnt(0)
	v_cmp_eq_u32_e32 vcc, v7, v44
	ds_bpermute_b32 v21, v3, v5 offset:12
	ds_bpermute_b32 v22, v3, v5 offset:20
	v_cndmask_b32_e32 v7, 0, v16, vcc
	v_cmp_eq_u32_e32 vcc, v17, v44
	ds_bpermute_b32 v17, v3, v8 offset:8
	s_nop 0
	v_cndmask_b32_e32 v16, 0, v18, vcc
	ds_bpermute_b32 v18, v3, v5 offset:8
	v_add_u32_e32 v7, v16, v7
	s_waitcnt lgkmcnt(0)
	v_cmp_eq_u32_e32 vcc, v17, v44
	s_nop 1
	v_cndmask_b32_e32 v16, 0, v18, vcc
	ds_bpermute_b32 v18, v3, v8 offset:16
	v_cmp_eq_u32_e32 vcc, v20, v44
	ds_bpermute_b32 v20, v3, v5 offset:16
	s_nop 0
	v_cndmask_b32_e32 v17, 0, v21, vcc
	ds_bpermute_b32 v21, v3, v8 offset:20
	s_waitcnt lgkmcnt(0)
	v_cmp_eq_u32_e32 vcc, v18, v44
	ds_bpermute_b32 v18, v3, v8 offset:24
	v_add3_u32 v7, v7, v16, v17
	v_cndmask_b32_e32 v16, 0, v20, vcc
	ds_bpermute_b32 v20, v3, v5 offset:24
	v_cmp_eq_u32_e32 vcc, v21, v44
	ds_bpermute_b32 v21, v3, v8 offset:28
	s_nop 0
	v_cndmask_b32_e32 v17, 0, v22, vcc
	ds_bpermute_b32 v22, v3, v5 offset:28
	s_waitcnt lgkmcnt(0)
	v_cmp_eq_u32_e32 vcc, v18, v44
	ds_bpermute_b32 v18, v3, v8 offset:32
	v_add3_u32 v7, v7, v16, v17
	v_cndmask_b32_e32 v16, 0, v20, vcc
	ds_bpermute_b32 v20, v3, v5 offset:32
	v_cmp_eq_u32_e32 vcc, v21, v44
	ds_bpermute_b32 v21, v3, v8 offset:36
	s_nop 0
	v_cndmask_b32_e32 v17, 0, v22, vcc
	ds_bpermute_b32 v22, v3, v5 offset:36
	s_waitcnt lgkmcnt(0)
	v_cmp_eq_u32_e32 vcc, v18, v44
	ds_bpermute_b32 v18, v3, v8 offset:40
	v_add3_u32 v7, v7, v16, v17
	v_cndmask_b32_e32 v16, 0, v20, vcc
	ds_bpermute_b32 v20, v3, v5 offset:40
	v_cmp_eq_u32_e32 vcc, v21, v44
	ds_bpermute_b32 v21, v3, v8 offset:44
	s_nop 0
	v_cndmask_b32_e32 v17, 0, v22, vcc
	ds_bpermute_b32 v22, v3, v5 offset:44
	s_waitcnt lgkmcnt(0)
	v_cmp_eq_u32_e32 vcc, v18, v44
	ds_bpermute_b32 v18, v3, v8 offset:48
	v_add3_u32 v7, v7, v16, v17
	v_cndmask_b32_e32 v16, 0, v20, vcc
	ds_bpermute_b32 v20, v3, v5 offset:48
	v_cmp_eq_u32_e32 vcc, v21, v44
	ds_bpermute_b32 v21, v3, v8 offset:52
	s_nop 0
	v_cndmask_b32_e32 v17, 0, v22, vcc
	ds_bpermute_b32 v22, v3, v5 offset:52
	s_waitcnt lgkmcnt(0)
	v_cmp_eq_u32_e32 vcc, v18, v44
	ds_bpermute_b32 v18, v3, v8 offset:56
	v_add3_u32 v7, v7, v16, v17
	v_cndmask_b32_e32 v16, 0, v20, vcc
	ds_bpermute_b32 v20, v3, v5 offset:56
	ds_bpermute_b32 v8, v3, v8 offset:60
	ds_bpermute_b32 v3, v3, v5 offset:60
	v_cmp_eq_u32_e32 vcc, v21, v44
	s_nop 1
	v_cndmask_b32_e32 v17, 0, v22, vcc
	s_waitcnt lgkmcnt(0)
	v_cmp_eq_u32_e32 vcc, v18, v44
	v_add3_u32 v5, v7, v16, v17
	v_mul_f32_e32 v17, 0x39000000, v19
	v_cndmask_b32_e32 v7, 0, v20, vcc
	v_cmp_eq_u32_e32 vcc, v8, v44
	s_nop 1
	v_cndmask_b32_e32 v3, 0, v3, vcc
	v_add3_u32 v5, v5, v7, v3
	v_mul_f32_e32 v3, v4, v19
	v_cvt_f32_i32_e32 v4, v5
	v_mov_b32_e32 v5, 0x2edbe6ff
	v_fmamk_f32 v7, v19, 0x39000000, v5
	v_cmp_gt_f32_e32 vcc, s13, v7
	v_fmac_f32_e32 v5, 0x39000000, v4
	v_mul_f32_e32 v16, 0x39000000, v4
	v_cndmask_b32_e64 v8, 0, 32, vcc
	v_ldexp_f32 v7, v7, v8
	v_log_f32_e32 v7, v7
	s_nop 0
	v_mul_f32_e32 v8, 0x3f317217, v7
	v_fma_f32 v8, v7, s12, -v8
	v_fmac_f32_e32 v8, 0x3377d1cf, v7
	v_fmac_f32_e32 v8, 0x3f317217, v7
	v_cmp_lt_f32_e64 s[2:3], |v7|, s14
	s_nop 1
	v_cndmask_b32_e64 v7, v7, v8, s[2:3]
	v_mov_b32_e32 v8, 0x41b17218
	v_cndmask_b32_e32 v18, 0, v8, vcc
	v_cmp_gt_f32_e32 vcc, s13, v5
	v_sub_f32_e32 v7, v7, v18
	v_cmp_gt_u32_e64 s[2:3], 16, v44
	v_cndmask_b32_e64 v4, 0, 32, vcc
	v_ldexp_f32 v4, v5, v4
	v_log_f32_e32 v4, v4
	v_mul_f32_e32 v5, v17, v7
	v_cndmask_b32_e64 v5, 0, v5, s[2:3]
	ds_bpermute_b32 v17, v11, v5
	v_mul_f32_e32 v7, 0x3f317217, v4
	v_fma_f32 v7, v4, s12, -v7
	v_fmac_f32_e32 v7, 0x3377d1cf, v4
	v_fmac_f32_e32 v7, 0x3f317217, v4
	v_cmp_lt_f32_e64 s[4:5], |v4|, s14
	s_waitcnt lgkmcnt(0)
	v_add_f32_e32 v17, v5, v17
	ds_bpermute_b32 v18, v12, v17
	v_cndmask_b32_e64 v4, v4, v7, s[4:5]
	v_cndmask_b32_e32 v7, 0, v8, vcc
	v_sub_f32_e32 v4, v4, v7
	v_mul_f32_e32 v4, v16, v4
	v_cndmask_b32_e64 v16, 0, v4, s[2:3]
	ds_bpermute_b32 v7, v11, v3
	ds_bpermute_b32 v11, v11, v16
	v_cmp_eq_u32_e32 vcc, 0, v44
	s_waitcnt lgkmcnt(0)
	v_pk_add_f32 v[2:3], v[2:3], v[6:7]
	v_add_f32_e32 v6, v16, v11
	ds_bpermute_b32 v4, v12, v2
	ds_bpermute_b32 v5, v12, v3
	ds_bpermute_b32 v11, v12, v6
	v_add_f32_e32 v7, v17, v18
	ds_bpermute_b32 v12, v13, v7
	s_waitcnt lgkmcnt(0)
	v_pk_add_f32 v[2:3], v[2:3], v[4:5]
	v_add_f32_e32 v6, v6, v11
	ds_bpermute_b32 v4, v13, v2
	ds_bpermute_b32 v5, v13, v3
	ds_bpermute_b32 v11, v13, v6
	v_add_f32_e32 v7, v7, v12
	ds_bpermute_b32 v12, v14, v7
	v_lshlrev_b32_e32 v13, 2, v10
	s_waitcnt lgkmcnt(0)
	v_pk_add_f32 v[2:3], v[2:3], v[4:5]
	v_add_f32_e32 v6, v6, v11
	ds_bpermute_b32 v4, v14, v2
	ds_bpermute_b32 v5, v14, v3
	ds_bpermute_b32 v10, v14, v6
	v_add_f32_e32 v7, v7, v12
	ds_bpermute_b32 v11, v15, v7
	s_waitcnt lgkmcnt(0)
	v_pk_add_f32 v[2:3], v[2:3], v[4:5]
	v_add_f32_e32 v10, v6, v10
	ds_bpermute_b32 v4, v15, v2
	ds_bpermute_b32 v5, v15, v3
	ds_bpermute_b32 v12, v15, v10
	v_add_f32_e32 v7, v7, v11
	ds_bpermute_b32 v6, v13, v9
	ds_bpermute_b32 v11, v13, v7
	s_waitcnt lgkmcnt(0)
	v_pk_add_f32 v[2:3], v[2:3], v[4:5]
	v_add_f32_e32 v10, v10, v12
	ds_bpermute_b32 v4, v13, v2
	ds_bpermute_b32 v5, v13, v3
	ds_bpermute_b32 v12, v13, v10
	s_and_saveexec_b64 s[6:7], vcc
	s_cbranch_execz .LBB4_46
	v_add_f32_e32 v7, v7, v11
	s_waitcnt lgkmcnt(0)
	v_pk_add_f32 v[2:3], v[2:3], v[4:5]
	s_mov_b32 s2, 0xbfb8aa3b
	v_mul_f32_e32 v5, 0xbfb8aa3b, v7
	v_add_f32_e32 v4, v9, v6
	v_fma_f32 v6, v7, s2, -v5
	v_rndne_f32_e32 v9, v5
	v_fmac_f32_e32 v6, 0xb2a5705f, v7
	v_sub_f32_e32 v5, v5, v9
	v_add_f32_e32 v5, v5, v6
	v_exp_f32_e32 v5, v5
	v_cvt_i32_f32_e32 v6, v9
	v_add_f32_e32 v10, v10, v12
	v_add_f32_e32 v2, v2, v3
	s_mov_b32 s3, 0x42ce8ed0
	v_ldexp_f32 v3, v5, v6
	v_mul_f32_e32 v5, 0xbfb8aa3b, v10
	v_fma_f32 v6, v10, s2, -v5
	v_rndne_f32_e32 v9, v5
	v_fmac_f32_e32 v6, 0xb2a5705f, v10
	v_sub_f32_e32 v5, v5, v9
	v_cmp_nlt_f32_e32 vcc, s3, v7
	s_mov_b32 s4, 0xc2b17218
	v_add_f32_e32 v5, v5, v6
	v_cndmask_b32_e32 v3, 0, v3, vcc
	v_exp_f32_e32 v5, v5
	v_cvt_i32_f32_e32 v6, v9
	v_mov_b32_e32 v9, 0x7f800000
	v_cmp_ngt_f32_e32 vcc, s4, v7
	v_cmp_nlt_f32_e64 s[2:3], s3, v10
	v_ldexp_f32 v5, v5, v6
	v_cndmask_b32_e32 v3, v9, v3, vcc
	v_add_f32_e32 v3, 0x2edbe6ff, v3
	v_cmp_gt_f32_e32 vcc, s13, v3
	v_cndmask_b32_e64 v5, 0, v5, s[2:3]
	v_cmp_ngt_f32_e64 s[2:3], s4, v10
	v_cndmask_b32_e64 v6, 0, 32, vcc
	v_ldexp_f32 v3, v3, v6
	v_log_f32_e32 v3, v3
	v_cndmask_b32_e64 v5, v9, v5, s[2:3]
	v_add_f32_e32 v5, 0x2edbe6ff, v5
	v_cmp_gt_f32_e64 s[2:3], s13, v5
	v_mul_f32_e32 v6, 0x3f317217, v3
	v_fma_f32 v6, v3, s12, -v6
	v_cndmask_b32_e64 v7, 0, 32, s[2:3]
	v_ldexp_f32 v5, v5, v7
	v_log_f32_e32 v5, v5
	v_fmac_f32_e32 v6, 0x3377d1cf, v3
	v_fmac_f32_e32 v6, 0x3f317217, v3
	v_cmp_lt_f32_e64 s[4:5], |v3|, s14
	v_mul_f32_e32 v2, 0x3fa00000, v2
	v_mul_f32_e32 v2, 0x34aaaaab, v2
	v_cndmask_b32_e64 v3, v3, v6, s[4:5]
	v_cndmask_b32_e32 v6, 0, v8, vcc
	v_sub_f32_e32 v3, v3, v6
	v_mul_f32_e32 v6, 0x3f317217, v5
	v_fma_f32 v6, v5, s12, -v6
	v_fmac_f32_e32 v6, 0x3377d1cf, v5
	v_fmac_f32_e32 v6, 0x3f317217, v5
	v_cmp_lt_f32_e64 vcc, |v5|, s14
	s_mov_b32 s4, 0x4a400000
	s_nop 0
	v_cndmask_b32_e32 v5, v5, v6, vcc
	v_cndmask_b32_e64 v6, 0, v8, s[2:3]
	v_div_scale_f32 v7, s[2:3], s4, s4, v4
	v_rcp_f32_e32 v8, v7
	v_sub_f32_e32 v5, v5, v6
	v_add_f32_e32 v3, v3, v5
	v_mul_f32_e32 v3, 0xbdcccccd, v3
	v_fma_f32 v5, -v7, v8, 1.0
	v_fmac_f32_e32 v8, v5, v8
	v_div_scale_f32 v5, vcc, v4, s4, v4
	v_mul_f32_e32 v6, v5, v8
	v_fma_f32 v9, -v7, v6, v5
	v_fmac_f32_e32 v6, v9, v8
	v_fma_f32 v5, -v7, v6, v5
	v_div_fmas_f32 v5, v5, v8, v6
	v_div_fixup_f32 v4, v5, s4, v4
	v_mov_b32_e32 v5, 0
	global_store_dword v5, v2, s[10:11] sc1
	global_store_dword v5, v3, s[10:11] offset:4 sc1
	global_store_dword v5, v4, s[10:11] offset:8 sc1

.LBB4_52:
	s_mul_hi_i32 s6, s16, 0x55555556
	s_lshr_b32 s2, s6, 31
	s_add_i32 s6, s6, s2
	s_add_i32 s5, s12, s6
	s_mov_b64 s[2:3], -1
	s_cmpk_lt_u32 s5, 0x80
	s_mul_i32 s5, s6, 0x120
	s_cbranch_scc0 .LBB4_54
	v_lshl_add_u32 v10, s6, 8, v50
	ds_read_b128 v[2:5], v10
	ds_read_b128 v[6:9], v10 offset:32
	s_mul_i32 s2, s6, 0xc0
	v_add_u32_e32 v76, s14, v53
	v_subrev_u32_e32 v76, s2, v76
	s_waitcnt lgkmcnt(0)
	v_mad_u32_u24 v5, v5, s13, v76
	v_mad_u32_u24 v4, v4, s13, v76
	v_mad_u32_u24 v7, v7, s13, v76
	v_mad_u32_u24 v6, v6, s13, v76
	v_mad_u32_u24 v9, v9, s13, v76
	v_mad_u32_u24 v8, v8, s13, v76
	v_mad_u32_u24 v3, v3, s13, v76
	v_mad_u32_u24 v2, v2, s13, v76
	ds_read_u16 v11, v4
	ds_read_u16 v12, v5
	ds_read_u16 v4, v8
	ds_read_u16 v5, v9
	ds_read_u16 v6, v6
	ds_read_u16 v7, v7
	ds_read_u16 v8, v2
	ds_read_u16 v9, v3
	s_waitcnt lgkmcnt(0)
	v_perm_b32 v21, v5, v4, s15
	ds_read_b128 v[2:5], v10 offset:64
	v_perm_b32 v20, v7, v6, s15
	v_perm_b32 v19, v12, v11, s15
	v_perm_b32 v18, v9, v8, s15
	ds_read_b128 v[6:9], v10 offset:96
	s_waitcnt lgkmcnt(0)
	v_mad_u32_u24 v2, v2, s13, v76
	v_mad_u32_u24 v3, v3, s13, v76
	v_mov_b32_e32 v11, v2
	v_mov_b32_e32 v2, v3
	v_mov_b32_e32 v12, v2
	v_mad_u32_u24 v2, v5, s13, v76
	v_mad_u32_u24 v3, v4, s13, v76
	v_mov_b32_e32 v13, v3
	v_mov_b32_e32 v14, v2
	v_mad_u32_u24 v2, v7, s13, v76
	v_mad_u32_u24 v3, v6, s13, v76
	v_mov_b32_e32 v6, v3
	v_mov_b32_e32 v7, v2
	v_mad_u32_u24 v2, v9, s13, v76
	v_mad_u32_u24 v3, v8, s13, v76
	v_mov_b32_e32 v8, v3
	v_mov_b32_e32 v9, v2
	ds_read_b128 v[2:5], v10 offset:128
	ds_read_u16 v11, v11
	ds_read_u16 v12, v12
	ds_read_u16 v13, v13
	ds_read_u16 v14, v14
	ds_read_u16 v15, v6
	ds_read_u16 v16, v7
	ds_read_u16 v17, v8
	ds_read_u16 v22, v9
	ds_read_b128 v[6:9], v10 offset:160
	s_waitcnt lgkmcnt(0)
	v_mad_u32_u24 v3, v3, s13, v76
	v_mad_u32_u24 v2, v2, s13, v76
	v_mad_u32_u24 v7, v7, s13, v76
	v_mad_u32_u24 v6, v6, s13, v76
	v_mad_u32_u24 v5, v5, s13, v76
	v_mad_u32_u24 v4, v4, s13, v76
	v_mad_u32_u24 v9, v9, s13, v76
	v_mad_u32_u24 v8, v8, s13, v76
	ds_read_u16 v23, v2
	ds_read_u16 v24, v3
	ds_read_u16 v25, v4
	ds_read_u16 v26, v5
	ds_read_u16 v6, v6
	ds_read_u16 v7, v7
	ds_read_u16 v2, v8
	ds_read_u16 v3, v9
	v_perm_b32 v41, v22, v17, s15
	s_waitcnt lgkmcnt(0)
	v_perm_b32 v35, v26, v25, s15
	v_perm_b32 v34, v24, v23, s15
	ds_read_b128 v[22:25], v10 offset:224
	v_perm_b32 v37, v3, v2, s15
	ds_read_b128 v[2:5], v10 offset:192
	v_perm_b32 v36, v7, v6, s15
	ds_read_b128 v[26:29], v54 offset:1024
	v_perm_b32 v40, v16, v15, s15
	v_perm_b32 v39, v14, v13, s15
	s_waitcnt lgkmcnt(0)
	v_mad_u32_u24 v2, v2, s13, v76
	v_mad_u32_u24 v3, v3, s13, v76
	v_mov_b32_e32 v30, v2
	v_mov_b32_e32 v2, v3
	v_mov_b32_e32 v31, v2
	v_mad_u32_u24 v2, v4, s13, v76
	v_mad_u32_u24 v6, v5, s13, v76
	v_mov_b32_e32 v32, v2
	ds_read_b128 v[2:5], v54
	v_mov_b32_e32 v33, v6
	v_mad_u32_u24 v6, v22, s13, v76
	v_perm_b32 v38, v12, v11, s15
	v_mov_b32_e32 v22, v6
	s_waitcnt lgkmcnt(0)
	v_mfma_f32_32x32x16_f16 v[2:17], v[2:5], v[18:21], 0
	v_mad_u32_u24 v23, v23, s13, v76
	v_mov_b32_e32 v55, v22
	v_mov_b32_e32 v22, v23
	v_mov_b32_e32 v56, v22
	v_mad_u32_u24 v57, v25, s13, v76
	v_mad_u32_u24 v58, v24, s13, v76
	ds_read_b128 v[22:25], v54 offset:2048
	v_mfma_f32_32x32x16_f16 v[2:17], v[26:29], v[38:41], v[2:17]
	v_mov_b32_e32 v26, v58
	v_mov_b32_e32 v58, v26
	v_mov_b32_e32 v26, v57
	v_mov_b32_e32 v57, v26
	ds_read_b128 v[26:29], v54 offset:3072
	s_waitcnt lgkmcnt(0)
	v_mfma_f32_32x32x16_f16 v[2:17], v[22:25], v[34:37], v[2:17]
	ds_read_u16 v22, v32
	ds_read_u16 v23, v33
	ds_read_u16 v24, v55
	ds_read_u16 v25, v58
	ds_read_u16 v32, v57
	ds_read_u16 v33, v56
	ds_read_u16 v30, v30
	ds_read_u16 v31, v31
	s_waitcnt lgkmcnt(0)
	v_perm_b32 v57, v23, v22, s15
	v_perm_b32 v59, v32, v25, s15
	v_perm_b32 v58, v33, v24, s15
	ds_read_b128 v[22:25], v54 offset:4096
	ds_read_b128 v[60:63], v54 offset:5120
	v_perm_b32 v56, v31, v30, s15
	ds_read_b128 v[64:67], v51
	ds_read_b128 v[68:71], v51 offset:32
	v_mfma_f32_32x32x16_f16 v[2:17], v[26:29], v[56:59], v[2:17]
	ds_read_b128 v[72:75], v54 offset:6144
	s_add_i32 s2, s5, 0
	s_waitcnt lgkmcnt(0)
	v_mfma_f32_32x32x16_f16 v[18:33], v[22:25], v[18:21], 0
	s_nop 7
	v_add_f32_e32 v55, v64, v2
	v_add_f32_e32 v64, v65, v3
	v_add_f32_e32 v65, v66, v4
	v_mul_f32_e32 v55, 0x3f7fffac, v55
	v_mfma_f32_32x32x16_f16 v[18:33], v[60:63], v[38:41], v[18:33]
	v_add_f32_e32 v39, v68, v6
	v_add_f32_e32 v40, v69, v7
	v_add_f32_e32 v41, v70, v8
	v_add_f32_e32 v60, v71, v9
	ds_read_b128 v[6:9], v54 offset:7168
	v_add_f32_e32 v38, v67, v5
	ds_read_b128 v[2:5], v51 offset:64
	v_mfma_f32_32x32x16_f16 v[18:33], v[72:75], v[34:37], v[18:33]
	ds_read_b128 v[34:37], v51 offset:96
	s_waitcnt lgkmcnt(0)
	v_add_f32_e32 v61, v2, v10
	v_add_f32_e32 v62, v3, v11
	v_add_f32_e32 v63, v4, v12
	v_add_f32_e32 v66, v5, v13
	v_mfma_f32_32x32x16_f16 v[18:33], v[6:9], v[56:59], v[18:33]
	ds_read_b128 v[2:5], v51 offset:128
	ds_read_b128 v[6:9], v51 offset:160
	v_add_f32_e32 v34, v34, v14
	v_add_f32_e32 v35, v35, v15
	v_add_f32_e32 v36, v36, v16
	v_add_f32_e32 v37, v37, v17
	v_mul_f32_e32 v59, 0x3f7fffac, v66
	s_waitcnt lgkmcnt(0)
	s_nop 3
	v_add_f32_e32 v18, v2, v18
	v_add_f32_e32 v19, v3, v19
	v_add_f32_e32 v20, v4, v20
	v_add_f32_e32 v21, v5, v21
	ds_read_b128 v[2:5], v51 offset:192
	v_add_f32_e32 v22, v6, v22
	v_add_f32_e32 v23, v7, v23
	v_add_f32_e32 v24, v8, v24
	v_add_f32_e32 v25, v9, v25
	ds_read_b128 v[6:9], v51 offset:224
	s_waitcnt lgkmcnt(0)
	v_add_f32_e32 v26, v2, v26
	v_add_f32_e32 v27, v3, v27
	v_add_f32_e32 v28, v4, v28
	v_add_f32_e32 v29, v5, v29
	ds_read_b128 v[2:5], v51 offset:256
	ds_read_b128 v[10:13], v51 offset:512
	v_add_f32_e32 v30, v6, v30
	v_add_f32_e32 v31, v7, v31
	v_add_f32_e32 v32, v8, v32
	v_add_f32_e32 v33, v9, v33
	ds_read_b128 v[6:9], v51 offset:288
	ds_read_b128 v[14:17], v51 offset:544
	s_waitcnt lgkmcnt(0)
	v_fma_f32 v55, v2, v55, v10
	v_mul_f32_e32 v2, 0x3f7fffac, v64
	v_fma_f32 v56, v3, v2, v11
	v_mul_f32_e32 v2, 0x3f7fffac, v65
	v_fma_f32 v57, v4, v2, v12
	v_mul_f32_e32 v2, 0x3f7fffac, v38
	v_fmac_f32_e32 v13, v5, v2
	v_mul_f32_e32 v2, 0x3f7fffac, v39
	v_fma_f32 v39, v6, v2, v14
	v_mul_f32_e32 v2, 0x3f7fffac, v40
	v_fma_f32 v40, v7, v2, v15
	v_mul_f32_e32 v2, 0x3f7fffac, v41
	v_fma_f32 v41, v8, v2, v16
	v_mul_f32_e32 v2, 0x3f7fffac, v60
	v_fmac_f32_e32 v17, v9, v2
	ds_read_b128 v[2:5], v51 offset:320
	ds_read_b128 v[6:9], v51 offset:576
	v_max_f32_e32 v38, 0, v13
	v_max_f32_e32 v58, 0, v17
	ds_read_b128 v[10:13], v51 offset:352
	ds_read_b128 v[14:17], v51 offset:608
	v_mul_f32_e32 v18, 0x3f7fffac, v18
	s_waitcnt lgkmcnt(0)
	v_fmac_f32_e32 v9, v5, v59
	v_mul_f32_e32 v5, 0x3f7fffac, v61
	v_fma_f32 v59, v2, v5, v6
	v_mul_f32_e32 v2, 0x3f7fffac, v62
	v_fma_f32 v60, v3, v2, v7
	v_mul_f32_e32 v2, 0x3f7fffac, v63
	v_fma_f32 v61, v4, v2, v8
	v_mul_f32_e32 v2, 0x3f7fffac, v34
	v_fma_f32 v34, v10, v2, v14
	v_mul_f32_e32 v2, 0x3f7fffac, v35
	v_fma_f32 v35, v11, v2, v15
	v_mul_f32_e32 v2, 0x3f7fffac, v36
	v_fma_f32 v36, v12, v2, v16
	v_mul_f32_e32 v2, 0x3f7fffac, v37
	v_max_f32_e32 v62, 0, v9
	v_fmac_f32_e32 v17, v13, v2
	ds_read_b128 v[2:5], v51 offset:384
	ds_read_b128 v[6:9], v51 offset:640
	v_max_f32_e32 v37, 0, v17
	ds_read_b128 v[10:13], v51 offset:416
	ds_read_b128 v[14:17], v51 offset:672
	v_mul_f32_e32 v26, 0x3f7fffac, v26
	v_mul_f32_e32 v29, 0x3f7fffac, v29
	s_waitcnt lgkmcnt(0)
	v_fma_f32 v18, v2, v18, v6
	v_mul_f32_e32 v2, 0x3f7fffac, v19
	v_fma_f32 v19, v3, v2, v7
	v_mul_f32_e32 v2, 0x3f7fffac, v20
	v_fma_f32 v20, v4, v2, v8
	v_mul_f32_e32 v2, 0x3f7fffac, v21
	v_fmac_f32_e32 v9, v5, v2
	v_mul_f32_e32 v2, 0x3f7fffac, v22
	v_fma_f32 v22, v10, v2, v14
	v_mul_f32_e32 v2, 0x3f7fffac, v23
	v_fma_f32 v23, v11, v2, v15
	v_mul_f32_e32 v2, 0x3f7fffac, v24
	v_fma_f32 v24, v12, v2, v16
	v_mul_f32_e32 v2, 0x3f7fffac, v25
	v_max_f32_e32 v21, 0, v9
	v_fmac_f32_e32 v17, v13, v2
	ds_read_b128 v[2:5], v51 offset:448
	ds_read_b128 v[6:9], v51 offset:704
	v_max_f32_e32 v25, 0, v17
	ds_read_b128 v[10:13], v51 offset:480
	ds_read_b128 v[14:17], v51 offset:736
	v_max_f32_e32 v39, 0, v39
	v_max_f32_e32 v40, 0, v40
	s_waitcnt lgkmcnt(0)
	v_fma_f32 v2, v2, v26, v6
	v_max_f32_e32 v6, 0, v2
	v_mul_f32_e32 v2, 0x3f7fffac, v27
	v_fma_f32 v2, v3, v2, v7
	v_max_f32_e32 v7, 0, v2
	v_mul_f32_e32 v2, 0x3f7fffac, v28
	v_fma_f32 v2, v4, v2, v8
	v_max_f32_e32 v8, 0, v2
	v_mul_f32_e32 v2, 0x3f7fffac, v30
	v_fma_f32 v2, v10, v2, v14
	v_max_f32_e32 v10, 0, v2
	v_mul_f32_e32 v2, 0x3f7fffac, v31
	v_fma_f32 v2, v11, v2, v15
	v_max_f32_e32 v11, 0, v2
	v_mul_f32_e32 v2, 0x3f7fffac, v32
	v_fma_f32 v2, v12, v2, v16
	v_fmac_f32_e32 v9, v5, v29
	v_max_f32_e32 v5, 0, v55
	v_max_f32_e32 v29, 0, v56
	v_max_f32_e32 v55, 0, v57
	v_max_f32_e32 v41, 0, v41
	v_max_f32_e32 v12, 0, v2
	v_mul_f32_e32 v2, 0x3f7fffac, v33
	v_add_u32_e32 v14, s2, v52
	v_max_f32_e32 v56, 0, v59
	v_max_f32_e32 v57, 0, v60
	v_max_f32_e32 v59, 0, v61
	v_max_f32_e32 v34, 0, v34
	v_max_f32_e32 v35, 0, v35
	v_max_f32_e32 v36, 0, v36
	v_fmac_f32_e32 v17, v13, v2
	v_add_u32_e32 v15, 0x14090, v14
	v_cvt_pkrtz_f16_f32 v2, v5, v29
	v_cvt_pkrtz_f16_f32 v3, v55, v38
	v_cvt_pkrtz_f16_f32 v4, v39, v40
	v_cvt_pkrtz_f16_f32 v5, v41, v58
	v_max_f32_e32 v18, 0, v18
	v_max_f32_e32 v19, 0, v19
	v_max_f32_e32 v20, 0, v20
	v_max_f32_e32 v22, 0, v22
	v_max_f32_e32 v23, 0, v23
	v_max_f32_e32 v24, 0, v24
	ds_write_b128 v15, v[2:5]
	v_cvt_pkrtz_f16_f32 v2, v56, v57
	v_cvt_pkrtz_f16_f32 v3, v59, v62
	v_cvt_pkrtz_f16_f32 v4, v34, v35
	v_cvt_pkrtz_f16_f32 v5, v36, v37
	v_add_u32_e32 v15, 0x140b0, v14
	v_max_f32_e32 v9, 0, v9
	v_max_f32_e32 v13, 0, v17
	ds_write_b128 v15, v[2:5]
	v_cvt_pkrtz_f16_f32 v2, v18, v19
	v_cvt_pkrtz_f16_f32 v3, v20, v21
	v_cvt_pkrtz_f16_f32 v4, v22, v23
	v_cvt_pkrtz_f16_f32 v5, v24, v25
	v_add_u32_e32 v15, 0x140d0, v14
	ds_write_b128 v15, v[2:5]
	v_cvt_pkrtz_f16_f32 v2, v6, v7
	v_cvt_pkrtz_f16_f32 v3, v8, v9
	v_cvt_pkrtz_f16_f32 v4, v10, v11
	v_cvt_pkrtz_f16_f32 v5, v12, v13
	v_add_u32_e32 v6, 0x140f0, v14
	ds_write_b128 v6, v[2:5]
	s_mov_b64 s[2:3], 0

.LBB4_63:
	s_or_b64 exec, exec, s[2:3]
	v_cmp_eq_u32_e32 vcc, 0, v0
	s_waitcnt lgkmcnt(0)
	s_barrier
	s_and_saveexec_b64 s[2:3], vcc
	s_cbranch_execz .LBB4_68
	s_add_i32 s2, 0, 0x23380
	v_mov_b32_e32 v0, s2
	ds_read_b128 v[0:3], v0
	s_add_i32 s2, 0, 0x23390
	v_mov_b32_e32 v4, s2
	ds_read_b64 v[4:5], v4
	s_mov_b64 s[6:7], exec
	s_waitcnt lgkmcnt(1)
	v_add_f32_e32 v0, v0, v1
	v_add_f32_e32 v0, v0, v2
	v_add_f32_e32 v0, v0, v3
	s_waitcnt lgkmcnt(0)
	v_add_f32_e32 v0, v0, v4
	v_add_f32_e32 v0, v0, v5
	v_mov_b32_e32 v1, 0.5
	v_fmamk_f32 v0, v0, 0x47800000, v1
	v_trunc_f32_e32 v0, v0
	v_mul_f32_e32 v1, 0x2f800000, v0
	v_floor_f32_e32 v1, v1
	v_fmamk_f32 v0, v1, 0xcf800000, v0
	v_cvt_u32_f32_e32 v0, v0
	v_cvt_u32_f32_e32 v1, v1
	s_mov_b32 s5, 0
	v_readfirstlane_b32 s2, v0
	v_readfirstlane_b32 s3, v1
	s_lshl_b64 s[2:3], s[2:3], 9
	s_or_b32 s2, s2, 1
	v_mov_b32_e32 v0, s2
	v_mov_b32_e32 v1, s3
	v_mov_b32_e32 v2, s45
	global_atomic_add_x2 v[0:1], v2, v[0:1], s[46:47] sc0
	s_waitcnt vmcnt(0)
	v_and_b32_e32 v2, 0x1ff, v0
	v_cmp_eq_u32_e32 vcc, 31, v2
	s_and_b64 exec, exec, vcc
	s_cbranch_execz .LBB4_68
	v_lshl_add_u64 v[0:1], s[2:3], 0, v[0:1]
	v_and_b32_e32 v0, 0xfffffe00, v0
	v_or_b32_e32 v0, 1, v0
	s_nop 0
	v_readfirstlane_b32 s2, v0
	v_readfirstlane_b32 s3, v1
	v_mov_b32_e32 v2, 0
	global_atomic_add_x2 v[0:1], v2, v[0:1], s[8:9] sc0
	s_waitcnt vmcnt(0)
	v_and_b32_e32 v2, 0x1ff, v0
	v_mov_b32_e32 v3, 0
	v_mov_b32_e32 v4, 0
	v_cmp_eq_u32_e32 vcc, 7, v2
	s_and_b64 exec, exec, vcc
	s_cbranch_execz .LBB4_68
	global_load_dword v6, v3, s[10:11] sc1
	global_load_dword v8, v3, s[10:11] offset:4 sc1
	global_load_dword v7, v3, s[10:11] offset:8 sc1
	v_mov_b32_e32 v2, v1
	v_mad_u64_u32 v[2:3], s[0:1], s3, v4, v[2:3]
	v_mov_b32_e32 v1, v2
	v_lshl_add_u64 v[0:1], s[2:3], 0, v[0:1]
	v_lshrrev_b64 v[0:1], 9, v[0:1]
	v_ffbh_u32_e32 v2, v1
	v_min_u32_e32 v2, 32, v2
	v_lshlrev_b64 v[0:1], v2, v[0:1]
	v_min_u32_e32 v0, 1, v0
	v_or_b32_e32 v0, v1, v0
	v_cvt_f32_u32_e32 v0, v0
	v_sub_u32_e32 v1, 32, v2
	s_mov_b32 s2, 0x47400000
	v_mov_b32_e32 v3, 0xc86000
	v_ldexp_f32 v0, v0, v1
	v_mul_f32_e32 v0, 0x37800000, v0
	v_div_scale_f32 v1, s[0:1], s2, s2, v0
	v_rcp_f32_e32 v2, v1
	v_div_scale_f32 v4, vcc, v0, s2, v0
	v_fma_f32 v5, -v1, v2, 1.0
	v_fmac_f32_e32 v2, v5, v2
	v_mul_f32_e32 v5, v4, v2
	v_fma_f32 v9, -v1, v5, v4
	v_fmac_f32_e32 v5, v9, v2
	v_fma_f32 v1, -v1, v5, v4
	v_div_fmas_f32 v1, v1, v2, v5
	v_div_fixup_f32 v5, v1, s2, v0
	s_waitcnt vmcnt(2)
	v_add_f32_e32 v0, v5, v6
	s_waitcnt vmcnt(0)
	v_fmamk_f32 v0, v7, 0x3dcccccd, v0
	v_add_f32_e32 v4, v0, v8
	global_store_dwordx4 v3, v[4:7], s[30:31]
	global_store_dword v3, v8, s[30:31] offset:16

	.amdhsa_kernel _Z7k5_convPKDF16_PKiS0_PKfS4_S4_S4_S4_S4_S4_S4_PfS4_S4_S2_S2_S4_PiS5_S5_
		.amdhsa_group_segment_fixed_size 0
		.amdhsa_private_segment_fixed_size 0
		.amdhsa_kernarg_size 416
		.amdhsa_user_sgpr_count 2
		.amdhsa_user_sgpr_dispatch_ptr 0
		.amdhsa_user_sgpr_queue_ptr 0
		.amdhsa_user_sgpr_kernarg_segment_ptr 1
		.amdhsa_user_sgpr_dispatch_id 0
		.amdhsa_user_sgpr_kernarg_preload_length 0
		.amdhsa_user_sgpr_kernarg_preload_offset 0
		.amdhsa_user_sgpr_private_segment_size 0
		.amdhsa_uses_dynamic_stack 0
		.amdhsa_enable_private_segment 0
		.amdhsa_system_sgpr_workgroup_id_x 1
		.amdhsa_system_sgpr_workgroup_id_y 0
		.amdhsa_system_sgpr_workgroup_id_z 0
		.amdhsa_system_sgpr_workgroup_info 0
		.amdhsa_system_vgpr_workitem_id 0
		.amdhsa_next_free_vgpr 88
		.amdhsa_next_free_sgpr 48
		.amdhsa_accum_offset 88
		.amdhsa_reserve_vcc 1
		.amdhsa_float_round_mode_32 0
		.amdhsa_float_round_mode_16_64 0
		.amdhsa_float_denorm_mode_32 3
		.amdhsa_float_denorm_mode_16_64 3
		.amdhsa_dx10_clamp 1
		.amdhsa_ieee_mode 1
		.amdhsa_fp16_overflow 0
		.amdhsa_tg_split 0
		.amdhsa_exception_fp_ieee_invalid_op 0
		.amdhsa_exception_fp_denorm_src 0
		.amdhsa_exception_fp_ieee_div_zero 0
		.amdhsa_exception_fp_ieee_overflow 0
		.amdhsa_exception_fp_ieee_underflow 0
		.amdhsa_exception_fp_ieee_inexact 0
		.amdhsa_exception_int_div_zero 0
	.end_amdhsa_kernel

amdhsa.kernels:
  - .agpr_count:     0
    .args:
      - .offset:         0
        .size:           272
        .value_kind:     by_value
    .group_segment_fixed_size: 27780
    .kernarg_segment_align: 8
    .kernarg_segment_size: 272
    .language:       OpenCL C
    .language_version:
      - 2
      - 0
    .max_flat_workgroup_size: 1024
    .name:           _Z6k_prep5PrepP
    .private_segment_fixed_size: 0
    .sgpr_count:     106
    .sgpr_spill_count: 0
    .symbol:         _Z6k_prep5PrepP.kd
    .uniform_work_group_size: 1
    .uses_dynamic_stack: false
    .vgpr_count:     135
    .vgpr_spill_count: 0
    .wavefront_size: 64
  - .agpr_count:     0
    .args:
      - .actual_access:  read_only
        .address_space:  global
        .offset:         0
        .size:           8
        .value_kind:     global_buffer
      - .actual_access:  read_only
        .address_space:  global
        .offset:         8
        .size:           8
        .value_kind:     global_buffer
      - .actual_access:  read_only
        .address_space:  global
        .offset:         16
        .size:           8
        .value_kind:     global_buffer
      - .address_space:  global
        .offset:         24
        .size:           8
        .value_kind:     global_buffer
      - .actual_access:  read_only
        .address_space:  global
        .offset:         32
        .size:           8
        .value_kind:     global_buffer
      - .actual_access:  read_only
        .address_space:  global
        .offset:         40
        .size:           8
        .value_kind:     global_buffer
      - .actual_access:  read_only
        .address_space:  global
        .offset:         48
        .size:           8
        .value_kind:     global_buffer
      - .actual_access:  read_only
        .address_space:  global
        .offset:         56
        .size:           8
        .value_kind:     global_buffer
      - .actual_access:  write_only
        .address_space:  global
        .offset:         64
        .size:           8
        .value_kind:     global_buffer
    .group_segment_fixed_size: 0
    .kernarg_segment_align: 8
    .kernarg_segment_size: 72
    .language:       OpenCL C
    .language_version:
      - 2
      - 0
    .max_flat_workgroup_size: 384
    .name:           _Z11k1_temporalPKfS0_S0_PKDF16_S0_S0_S0_S0_Pf
    .private_segment_fixed_size: 0
    .sgpr_count:     34
    .sgpr_spill_count: 0
    .symbol:         _Z11k1_temporalPKfS0_S0_PKDF16_S0_S0_S0_S0_Pf.kd
    .uniform_work_group_size: 1
    .uses_dynamic_stack: false
    .vgpr_count:     247
    .vgpr_spill_count: 0
    .wavefront_size: 64
  - .agpr_count:     0
    .args:
      - .address_space:  global
        .offset:         0
        .size:           8
        .value_kind:     global_buffer
      - .address_space:  global
        .offset:         8
        .size:           8
        .value_kind:     global_buffer
      - .actual_access:  read_only
        .address_space:  global
        .offset:         16
        .size:           8
        .value_kind:     global_buffer
      - .actual_access:  read_only
        .address_space:  global
        .offset:         24
        .size:           8
        .value_kind:     global_buffer
      - .actual_access:  read_only
        .address_space:  global
        .offset:         32
        .size:           8
        .value_kind:     global_buffer
      - .actual_access:  read_only
        .address_space:  global
        .offset:         40
        .size:           8
        .value_kind:     global_buffer
      - .actual_access:  read_only
        .address_space:  global
        .offset:         48
        .size:           8
        .value_kind:     global_buffer
      - .actual_access:  read_only
        .address_space:  global
        .offset:         56
        .size:           8
        .value_kind:     global_buffer
      - .actual_access:  read_only
        .address_space:  global
        .offset:         64
        .size:           8
        .value_kind:     global_buffer
      - .actual_access:  read_only
        .address_space:  global
        .offset:         72
        .size:           8
        .value_kind:     global_buffer
      - .actual_access:  read_only
        .address_space:  global
        .offset:         80
        .size:           8
        .value_kind:     global_buffer
      - .actual_access:  read_only
        .address_space:  global
        .offset:         88
        .size:           8
        .value_kind:     global_buffer
      - .actual_access:  read_only
        .address_space:  global
        .offset:         96
        .size:           8
        .value_kind:     global_buffer
      - .actual_access:  read_only
        .address_space:  global
        .offset:         104
        .size:           8
        .value_kind:     global_buffer
      - .actual_access:  read_only
        .address_space:  global
        .offset:         112
        .size:           8
        .value_kind:     global_buffer
      - .actual_access:  read_only
        .address_space:  global
        .offset:         120
        .size:           8
        .value_kind:     global_buffer
      - .address_space:  global
        .offset:         128
        .size:           8
        .value_kind:     global_buffer
      - .actual_access:  write_only
        .address_space:  global
        .offset:         136
        .size:           8
        .value_kind:     global_buffer
      - .actual_access:  write_only
        .address_space:  global
        .offset:         144
        .size:           8
        .value_kind:     global_buffer
      - .actual_access:  write_only
        .address_space:  global
        .offset:         152
        .size:           8
        .value_kind:     global_buffer
      - .actual_access:  write_only
        .address_space:  global
        .offset:         160
        .size:           8
        .value_kind:     global_buffer
    .group_segment_fixed_size: 0
    .kernarg_segment_align: 8
    .kernarg_segment_size: 168
    .language:       OpenCL C
    .language_version:
      - 2
      - 0
    .max_flat_workgroup_size: 512
    .name:           _Z10k2_featurePKfPKDF16_S0_S0_S0_S0_S0_S0_PKyS0_S0_S0_S0_S0_S0_S0_PfS5_S5_S5_S5_
    .private_segment_fixed_size: 0
    .sgpr_count:     38
    .sgpr_spill_count: 0
    .symbol:         _Z10k2_featurePKfPKDF16_S0_S0_S0_S0_S0_S0_PKyS0_S0_S0_S0_S0_S0_S0_PfS5_S5_S5_S5_.kd
    .uniform_work_group_size: 1
    .uses_dynamic_stack: false
    .vgpr_count:     256
    .vgpr_spill_count: 0
    .wavefront_size: 64
  - .agpr_count:     0
    .args:
      - .actual_access:  read_only
        .address_space:  global
        .offset:         0
        .size:           8
        .value_kind:     global_buffer
      - .actual_access:  read_only
        .address_space:  global
        .offset:         8
        .size:           8
        .value_kind:     global_buffer
      - .actual_access:  read_only
        .address_space:  global
        .offset:         16
        .size:           8
        .value_kind:     global_buffer
      - .actual_access:  read_only
        .address_space:  global
        .offset:         24
        .size:           8
        .value_kind:     global_buffer
      - .actual_access:  read_only
        .address_space:  global
        .offset:         32
        .size:           8
        .value_kind:     global_buffer
      - .actual_access:  write_only
        .address_space:  global
        .offset:         40
        .size:           8
        .value_kind:     global_buffer
      - .actual_access:  write_only
        .address_space:  global
        .offset:         48
        .size:           8
        .value_kind:     global_buffer
      - .address_space:  global
        .offset:         56
        .size:           8
        .value_kind:     global_buffer
      - .actual_access:  write_only
        .address_space:  global
        .offset:         64
        .size:           8
        .value_kind:     global_buffer
    .group_segment_fixed_size: 56768
    .kernarg_segment_align: 8
    .kernarg_segment_size: 72
    .language:       OpenCL C
    .language_version:
      - 2
      - 0
    .max_flat_workgroup_size: 768
    .name:           _Z5k3_vqPKDF16_S0_S0_S0_PKfPiPfS3_S4_
    .private_segment_fixed_size: 0
    .sgpr_count:     54
    .sgpr_spill_count: 0
    .symbol:         _Z5k3_vqPKDF16_S0_S0_S0_PKfPiPfS3_S4_.kd
    .uniform_work_group_size: 1
    .uses_dynamic_stack: false
    .vgpr_count:     76
    .vgpr_spill_count: 0
    .wavefront_size: 64
  - .agpr_count:     0
    .args:
      - .actual_access:  read_only
        .address_space:  global
        .offset:         0
        .size:           8
        .value_kind:     global_buffer
      - .actual_access:  read_only
        .address_space:  global
        .offset:         8
        .size:           8
        .value_kind:     global_buffer
      - .address_space:  global
        .offset:         16
        .size:           8
        .value_kind:     global_buffer
      - .actual_access:  read_only
        .address_space:  global
        .offset:         24
        .size:           8
        .value_kind:     global_buffer
      - .actual_access:  read_only
        .address_space:  global
        .offset:         32
        .size:           8
        .value_kind:     global_buffer
      - .actual_access:  read_only
        .address_space:  global
        .offset:         40
        .size:           8
        .value_kind:     global_buffer
      - .actual_access:  read_only
        .address_space:  global
        .offset:         48
        .size:           8
        .value_kind:     global_buffer
      - .actual_access:  read_only
        .address_space:  global
        .offset:         56
        .size:           8
        .value_kind:     global_buffer
      - .actual_access:  read_only
        .address_space:  global
        .offset:         64
        .size:           8
        .value_kind:     global_buffer
      - .actual_access:  read_only
        .address_space:  global
        .offset:         72
        .size:           8
        .value_kind:     global_buffer
      - .actual_access:  read_only
        .address_space:  global
        .offset:         80
        .size:           8
        .value_kind:     global_buffer
      - .address_space:  global
        .offset:         88
        .size:           8
        .value_kind:     global_buffer
      - .actual_access:  read_only
        .address_space:  global
        .offset:         96
        .size:           8
        .value_kind:     global_buffer
      - .actual_access:  read_only
        .address_space:  global
        .offset:         104
        .size:           8
        .value_kind:     global_buffer
      - .actual_access:  read_only
        .address_space:  global
        .offset:         112
        .size:           8
        .value_kind:     global_buffer
      - .actual_access:  read_only
        .address_space:  global
        .offset:         120
        .size:           8
        .value_kind:     global_buffer
      - .actual_access:  read_only
        .address_space:  global
        .offset:         128
        .size:           8
        .value_kind:     global_buffer
      - .address_space:  global
        .offset:         136
        .size:           8
        .value_kind:     global_buffer
      - .address_space:  global
        .offset:         144
        .size:           8
        .value_kind:     global_buffer
      - .actual_access:  write_only
        .address_space:  global
        .offset:         152
        .size:           8
        .value_kind:     global_buffer
      - .offset:         160
        .size:           4
        .value_kind:     hidden_block_count_x
      - .offset:         164
        .size:           4
        .value_kind:     hidden_block_count_y
      - .offset:         168
        .size:           4
        .value_kind:     hidden_block_count_z
      - .offset:         172
        .size:           2
        .value_kind:     hidden_group_size_x
      - .offset:         174
        .size:           2
        .value_kind:     hidden_group_size_y
      - .offset:         176
        .size:           2
        .value_kind:     hidden_group_size_z
      - .offset:         178
        .size:           2
        .value_kind:     hidden_remainder_x
      - .offset:         180
        .size:           2
        .value_kind:     hidden_remainder_y
      - .offset:         182
        .size:           2
        .value_kind:     hidden_remainder_z
      - .offset:         200
        .size:           8
        .value_kind:     hidden_global_offset_x
      - .offset:         208
        .size:           8
        .value_kind:     hidden_global_offset_y
      - .offset:         216
        .size:           8
        .value_kind:     hidden_global_offset_z
      - .offset:         224
        .size:           2
        .value_kind:     hidden_grid_dims
      - .offset:         280
        .size:           4
        .value_kind:     hidden_dynamic_lds_size
    .group_segment_fixed_size: 0
    .kernarg_segment_align: 8
    .kernarg_segment_size: 416
    .language:       OpenCL C
    .language_version:
      - 2
      - 0
    .max_flat_workgroup_size: 768
    .name:           _Z7k5_convPKDF16_PKiS0_PKfS4_S4_S4_S4_S4_S4_S4_PfS4_S4_S2_S2_S4_PiS5_S5_
    .private_segment_fixed_size: 0
    .sgpr_count:     54
    .sgpr_spill_count: 0
    .symbol:         _Z7k5_convPKDF16_PKiS0_PKfS4_S4_S4_S4_S4_S4_S4_PfS4_S4_S2_S2_S4_PiS5_S5_.kd
    .uniform_work_group_size: 1
    .uses_dynamic_stack: false
    .vgpr_count:     88
    .vgpr_spill_count: 0
    .wavefront_size: 64
